# v85 + MoE item set-up: one-LDS-trip fast path (experts with 1-2 row tiles) instead of 2 trips + integer division; thread-id table entry requested before the lookup
# speedup vs baseline: 1.0050x; 1.0050x over previous
.LBB0_777:
	s_add_i32 s44, s22, s3
	s_cmp_lt_i32 s44, s2
	s_cselect_b64 s[18:19], -1, 0
	s_cmp_ge_i32 s44, s2
	s_cselect_b64 s[0:1], -1, 0
	s_and_b64 vcc, exec, s[0:1]
	s_mov_b32 s8, s6
	s_mov_b32 s45, s7
	s_mov_b32 s46, s23
	v_mov_b32_e32 v176, v166
	s_waitcnt lgkmcnt(5)
	v_mov_b32_e32 v175, v139
	s_getreg_b32 s10, hwreg(HW_REG_HW_ID, 0, 6)
	s_lshl_b32 s10, s10, 2
	s_add_i32 s10, s10, 0x27000
	v_mov_b32_e32 v177, s10
	ds_read_b32 v177, v177
	s_cbranch_vccnz .LBB0_781
	v_mbcnt_lo_u32_b32 v52, -1, 0
	v_mbcnt_hi_u32_b32 v52, -1, v52
	v_lshlrev_b32_e32 v52, 4, v52
	v_add_u32_e32 v52, 0x1f024, v52
	ds_read_b32 v53, v52
	ds_read_b32 v175, v52 offset:4
	ds_read_b32 v176, v52 offset:8
	ds_read_b32 v52, v52 offset:12
	s_ashr_i32 s9, s44, 2
	s_waitcnt lgkmcnt(0)
	v_cmp_ge_i32_e64 s[10:11], s9, v53
	v_cmp_ge_i32_e64 s[12:13], s9, v175
	s_bcnt1_i32_b64 s8, s[10:11]
	s_bcnt1_i32_b64 s10, s[12:13]
	s_add_i32 s8, s8, s10
	v_cmp_ge_i32_e64 s[10:11], s9, v176
	v_cmp_ge_i32_e64 s[12:13], s9, v52
	s_bcnt1_i32_b64 s10, s[10:11]
	s_bcnt1_i32_b64 s12, s[12:13]
	s_add_i32 s8, s8, s10
	s_add_i32 s8, s8, s12
	s_lshl_b32 s9, s8, 2
	s_add_i32 s9, s9, 0x1e800
	v_mov_b32_e32 v52, s9
	ds_read_b32 v53, v52
	ds_read_b32 v175, v52 offset:1040
	ds_read_b32 v176, v52 offset:2080
	ds_read_b32 v52, v52 offset:2084
	s_waitcnt lgkmcnt(0)
	v_readfirstlane_b32 s9, v176
	v_readfirstlane_b32 s10, v52
	v_readfirstlane_b32 s11, v53
	s_sub_i32 s10, s10, s9
	s_cmp_gt_u32 s10, 2
	s_cbranch_scc1 .Lopt24_m10_orig
	s_lshl_b32 s9, s9, 2
	s_sub_i32 s9, s44, s9
	s_and_b32 s45, s9, 3
	s_lshr_b32 s9, s9, 2
	s_add_i32 s11, s11, s10
	s_add_i32 s11, s11, -1
	s_add_i32 s10, s10, -1
	s_lshr_b32 s11, s11, s10
	s_mul_i32 s46, s9, s11
	s_add_i32 s11, s46, s11
	v_min_i32_e32 v176, s11, v53
	s_branch .LBB0_781
.Lopt24_m10_orig:
	s_lshl_b32 s9, s8, 2
	s_add_i32 s9, s9, 0
	s_add_i32 s10, s9, 0x1f020
	v_mov_b32_e32 v52, s10
	ds_read2_b32 v[52:53], v52 offset1:1
	s_add_i32 s14, s9, 0x1e800
	s_add_i32 s9, s9, 0x1ec10
	s_waitcnt lgkmcnt(0)
	v_readfirstlane_b32 s10, v52
	v_mov_b32_e32 v52, s14
	ds_read_b32 v52, v52
	v_readfirstlane_b32 s11, v53
	s_sub_i32 s11, s11, s10
	s_lshl_b32 s10, s10, 2
	s_sub_i32 s10, s44, s10
	s_ashr_i32 s12, s10, 31
	v_mov_b32_e32 v53, s9
	s_lshr_b32 s12, s12, 30
	ds_read_b32 v175, v53
	s_waitcnt lgkmcnt(1)
	v_readfirstlane_b32 s9, v52
	s_add_i32 s12, s10, s12
	s_add_i32 s9, s9, s11
	s_ashr_i32 s13, s12, 2
	s_and_b32 s12, s12, -4
	s_add_i32 s9, s9, -1
	s_sub_i32 s45, s10, s12
	s_xor_b32 s10, s9, s11
	s_abs_i32 s11, s11
	v_cvt_f32_u32_e32 v53, s11
	s_sub_i32 s12, 0, s11
	s_abs_i32 s9, s9
	s_ashr_i32 s10, s10, 31
	v_rcp_iflag_f32_e32 v53, v53
	s_nop 0
	v_mul_f32_e32 v53, 0x4f7ffffe, v53
	v_cvt_u32_f32_e32 v53, v53
	s_nop 0
	v_readfirstlane_b32 s14, v53
	s_mul_i32 s12, s12, s14
	s_mul_hi_u32 s12, s14, s12
	s_add_i32 s14, s14, s12
	s_mul_hi_u32 s12, s9, s14
	s_mul_i32 s14, s12, s11
	s_sub_i32 s9, s9, s14
	s_add_i32 s14, s12, 1
	s_sub_i32 s15, s9, s11
	s_cmp_ge_u32 s9, s11
	s_cselect_b32 s12, s14, s12
	s_cselect_b32 s9, s15, s9
	s_add_i32 s14, s12, 1
	s_cmp_ge_u32 s9, s11
	s_cselect_b32 s9, s14, s12
	s_xor_b32 s9, s9, s10
	s_sub_i32 s9, s9, s10
	s_mul_i32 s46, s13, s9
	s_add_i32 s9, s46, s9
	v_min_i32_e32 v176, s9, v52
.LBB0_781:
	s_waitcnt lgkmcnt(0)
	v_mov_b32_e32 v52, v177
	v_cndmask_b32_e64 v177, 0, 1, s[18:19]
	v_mov_b32_e32 v53, v133
	v_readfirstlane_b32 s9, v177
	s_xor_b32 s47, s24, s9
	s_waitcnt lgkmcnt(0)
	v_readfirstlane_b32 s9, v52
	v_mbcnt_lo_u32_b32 v52, -1, v53
	v_mbcnt_hi_u32_b32 v52, -1, v52
	v_lshl_or_b32 v52, s9, 6, v52
	s_waitcnt vmcnt(7)
	v_cvt_pk_bf16_f32 v20, v20, v21
	v_lshrrev_b32_e32 v55, 3, v52
	v_lshlrev_b32_e32 v56, 4, v52
	v_and_b32_e32 v56, 0x70, v56
	v_mul_lo_u32 v55, v55, s29
	v_ashrrev_i32_e32 v54, 5, v52
	v_add3_u32 v57, 0, v56, v55
	ds_write_b128 v57, v[36:39]
	ds_write_b128 v57, v[32:35] offset:9216
	s_waitcnt vmcnt(6)
	ds_write_b128 v57, v[44:47] offset:18432
	s_waitcnt vmcnt(5)
	ds_write_b128 v57, v[40:43] offset:27648
	s_waitcnt vmcnt(4)
	ds_write_b128 v57, v[48:51] offset:36864
	v_lshrrev_b32_e32 v34, 1, v54
	v_bfe_u32 v32, v52, 2, 3
	v_and_b32_e32 v33, 3, v54
	v_and_b32_e32 v34, 4, v34
	v_bitop3_b32 v32, v34, v32, v33 bitop3:0x36
	v_lshlrev_b32_e32 v33, 2, v52
	v_and_b32_e32 v57, 12, v33
	v_lshlrev_b32_e32 v58, 1, v57
	v_lshl_or_b32 v59, v32, 5, v58
	v_lshlrev_b32_e32 v54, 8, v54
	v_cvt_pk_bf16_f32 v21, v22, v23
	v_add3_u32 v22, s33, v59, v54
	s_waitcnt vmcnt(6)
	v_cvt_pk_bf16_f32 v16, v16, v17
	v_cvt_pk_bf16_f32 v17, v18, v19
	ds_write2st64_b64 v22, v[20:21], v[16:17] offset1:8
	s_waitcnt vmcnt(5)
	v_cvt_pk_bf16_f32 v16, v28, v29
	v_cvt_pk_bf16_f32 v17, v30, v31
	s_waitcnt vmcnt(4)
	v_cvt_pk_bf16_f32 v18, v24, v25
	v_cvt_pk_bf16_f32 v19, v26, v27
	s_mul_i32 s9, s24, 0x2800
	ds_write2st64_b64 v22, v[16:17], v[18:19] offset0:16 offset1:24
	v_add_u32_e32 v16, s9, v174
	v_add_u32_e32 v217, s9, v168
	v_add_u32_e32 v218, 48, v16
	ds_read_b32 v132, v217
	ds_read2st64_b32 v[16:17], v218 offset0:20 offset1:28
	ds_read2st64_b32 v[22:23], v218 offset0:36 offset1:44
	v_bfe_u32 v25, v52, 2, 2
	v_bfe_u32 v26, v52, 6, 1
	s_waitcnt lgkmcnt(2)
	v_lshl_add_u64 v[18:19], v[132:133], 1, s[92:93]
	s_waitcnt lgkmcnt(1)
	v_mov_b32_e32 v132, v16
	v_lshl_add_u64 v[20:21], v[132:133], 1, s[92:93]
	v_mov_b32_e32 v132, v17
	v_lshl_add_u64 v[16:17], v[132:133], 1, s[92:93]
	s_waitcnt lgkmcnt(0)
	v_mov_b32_e32 v132, v22
	global_load_dwordx4 v[32:35], v[18:19], off offset:128
	global_load_dwordx4 v[36:39], v[20:21], off offset:128
	v_lshl_add_u64 v[18:19], v[132:133], 1, s[92:93]
	v_mov_b32_e32 v132, v23
	global_load_dwordx4 v[44:47], v[16:17], off offset:128
	global_load_dwordx4 v[48:51], v[18:19], off offset:128
	v_lshl_add_u64 v[16:17], v[132:133], 1, s[92:93]
	global_load_dwordx4 v[40:43], v[16:17], off offset:128
	v_lshrrev_b32_e32 v18, 2, v52
	v_and_b32_e32 v18, 4, v18
	v_lshrrev_b32_e32 v16, 1, v52
	v_or_b32_e32 v19, v18, v25
	v_and_b32_e32 v16, 24, v16
	v_lshlrev_b32_e32 v20, 6, v26
	v_lshlrev_b32_e32 v19, 4, v19
	v_lshlrev_b32_e32 v23, 2, v26
	v_or_b32_e32 v17, v16, v25
	v_xor_b32_e32 v19, v19, v20
	v_or_b32_e32 v26, 1, v23
	v_or_b32_e32 v27, 2, v23
	v_or_b32_e32 v23, 3, v23
	v_or_b32_e32 v19, v19, v57
	v_lshlrev_b32_e32 v17, 8, v17
	v_bitop3_b32 v26, v18, v26, v25 bitop3:0x36
	v_bitop3_b32 v27, v18, v27, v25 bitop3:0x36
	v_bitop3_b32 v18, v18, v23, v25 bitop3:0x36
	s_lshl_b32 s10, s7, 6
	v_ashrrev_i32_e32 v53, 7, v52
	v_add_u32_e32 v20, s33, v17
	v_lshlrev_b32_e32 v19, 1, v19
	v_lshl_or_b32 v26, v26, 5, v58
	v_lshl_or_b32 v27, v27, 5, v58
	v_lshl_or_b32 v18, v18, 5, v58
	s_ashr_i32 s11, s10, 31
	v_and_b32_e32 v24, 15, v52
	v_add_u32_e32 v213, v20, v19
	v_add_u32_e32 v214, v20, v26
	v_add_u32_e32 v211, v20, v27
	v_add_u32_e32 v145, v20, v18
	v_mul_lo_u32 v20, v53, s28
	s_cmpk_lt_i32 s8, 0x100
	v_add_u32_e32 v21, 0, v17
	v_or_b32_e32 v20, v20, v24
	s_cselect_b64 s[12:13], -1, 0
	s_cmpk_gt_i32 s8, 0xff
	v_add_u32_e32 v22, 0x16c00, v21
	v_lshlrev_b32_e32 v16, 1, v16
	v_mul_lo_u32 v20, v20, s29
	s_cselect_b64 s[14:15], -1, 0
	s_ashr_i32 s9, s8, 31
	v_add_u32_e32 v216, v22, v19
	v_add_u32_e32 v215, v22, v26
	v_add_u32_e32 v212, v22, v27
	v_add_u32_e32 v147, v22, v18
	v_add3_u32 v178, 0, v16, v20
	v_add3_u32 v16, 0, v54, v59
	v_add_u32_e32 v22, 0x18c00, v21
	s_lshl_b64 s[16:17], s[8:9], 16
	v_add_u32_e32 v209, 0x1b800, v16
	v_add_u32_e32 v208, 0x1c800, v16
	v_add_u32_e32 v206, 0x1d800, v16
	v_or_b32_e32 v20, 0x2000, v17
	v_add_u32_e32 v207, v22, v19
	v_add_u32_e32 v204, v22, v26
	v_add_u32_e32 v201, v22, v27
	v_add_u32_e32 v199, v22, v18
	v_add_u32_e32 v22, 0x1ac00, v21
	v_add_u32_e32 v220, 0x17800, v16
	v_add_u32_e32 v221, 0x18800, v16
	v_add_u32_e32 v222, 0x19800, v16
	v_add_u32_e32 v16, 0x1cc00, v21
	s_cmpk_lt_i32 s6, 0x100
	v_add_u32_e32 v21, s46, v141
	v_readlane_b32 s76, v253, 4
	v_add3_u32 v205, s33, v19, v20
	v_add3_u32 v203, s33, v26, v20
	v_add3_u32 v200, s33, v27, v20
	v_add3_u32 v198, s33, v18, v20
	v_add_u32_e32 v17, s42, v17
	v_add_u32_e32 v194, v22, v19
	v_add_u32_e32 v191, v22, v26
	v_add_u32_e32 v189, v22, v27
	v_add_u32_e32 v188, v22, v18
	v_add3_u32 v185, s42, v19, v20
	v_add3_u32 v183, s42, v26, v20
	v_add3_u32 v181, s42, v27, v20
	v_add3_u32 v179, s42, v18, v20
	v_add_u32_e32 v20, -1, v176
	v_add_u32_e32 v22, 0x80, v21
	s_cselect_b32 s20, s6, 0
	v_readlane_b32 s78, v253, 6
	v_readlane_b32 s79, v253, 7
	v_readlane_b32 s80, v253, 8
	v_readlane_b32 s81, v253, 9
	v_readlane_b32 s84, v253, 12
	v_readlane_b32 s85, v253, 13
	v_readlane_b32 s86, v253, 14
	v_readlane_b32 s87, v253, 15
	v_add_u32_e32 v187, v17, v18
	v_add_u32_e32 v186, v16, v19
	v_add_u32_e32 v184, v16, v26
	v_add_u32_e32 v182, v16, v27
	v_add_u32_e32 v180, v16, v18
	v_min_i32_e32 v16, v21, v20
	v_add_u32_e32 v18, 64, v21
	v_min_i32_e32 v148, v22, v20
	v_add_u32_e32 v22, 0xc0, v21
	v_add_u32_e32 v21, 0x100, v21
	s_cselect_b32 s50, s78, s84
	s_cselect_b32 s51, s79, s85
	s_cselect_b32 s52, s80, s86
	s_cselect_b32 s53, s81, s87
	s_ashr_i32 s21, s20, 31
	v_min_i32_e32 v150, v22, v20
	v_min_i32_e32 v152, v21, v20
	s_lshl_b64 s[20:21], s[20:21], 20
	v_mov_b32_e32 v21, s51
	v_mov_b32_e32 v22, s50
	v_readlane_b32 s50, v253, 61
	v_min_i32_e32 v18, v18, v20
	v_readlane_b32 s51, v253, 62
	s_add_u32 s16, s50, s16
	v_add_u32_e32 v193, v17, v19
	v_add_u32_e32 v190, v17, v26
	v_add_u32_e32 v192, v17, v27
	v_ashrrev_i32_e32 v17, 31, v16
	v_ashrrev_i32_e32 v19, 31, v18
	v_ashrrev_i32_e32 v149, 31, v148
	v_ashrrev_i32_e32 v151, 31, v150
	v_ashrrev_i32_e32 v153, 31, v152
	v_mov_b32_e32 v20, s53
	s_addc_u32 s17, s51, s17
	v_cndmask_b32_e64 v21, v20, v21, s[4:5]
	v_mov_b32_e32 v20, s52
	v_lshl_add_u64 v[154:155], v[16:17], 2, s[16:17]
	v_lshl_add_u64 v[156:157], v[18:19], 2, s[16:17]
	v_lshl_add_u64 v[158:159], v[148:149], 2, s[16:17]
	v_lshl_add_u64 v[160:161], v[150:151], 2, s[16:17]
	v_lshl_add_u64 v[162:163], v[152:153], 2, s[16:17]
	s_and_b64 s[98:99], s[18:19], s[12:13]
	s_cbranch_scc0 .Lopt1_m10_skip
	global_load_dword v224, v[154:155], off
	global_load_dword v225, v[156:157], off
	global_load_dword v226, v[158:159], off
	global_load_dword v227, v[160:161], off
	global_load_dword v228, v[162:163], off

.LBB0_902:
	s_add_i32 s23, s12, s1
	s_cmp_lt_i32 s23, s0
	s_cselect_b64 s[4:5], -1, 0
	s_cmp_ge_i32 s23, s0
	s_cselect_b64 s[2:3], -1, 0
	s_and_b64 vcc, exec, s[2:3]
	s_mov_b32 s24, s13
	s_mov_b32 s25, s15
	s_mov_b32 s26, s14
	v_mov_b32_e32 v163, v156
	v_mov_b32_e32 v162, v141
	s_getreg_b32 s6, hwreg(HW_REG_HW_ID, 0, 6)
	s_lshl_b32 s6, s6, 2
	s_add_i32 s6, s6, 0x27000
	v_mov_b32_e32 v244, s6
	ds_read_b32 v244, v244
	s_cbranch_vccnz .LBB0_906
	v_mbcnt_lo_u32_b32 v52, -1, 0
	v_mbcnt_hi_u32_b32 v52, -1, v52
	v_lshlrev_b32_e32 v52, 4, v52
	v_add_u32_e32 v52, 0x1f024, v52
	ds_read_b32 v53, v52
	ds_read_b32 v162, v52 offset:4
	ds_read_b32 v163, v52 offset:8
	ds_read_b32 v52, v52 offset:12
	s_ashr_i32 s6, s23, 3
	s_waitcnt lgkmcnt(0)
	v_cmp_ge_i32_e64 s[8:9], s6, v53
	v_cmp_ge_i32_e64 s[10:11], s6, v162
	s_bcnt1_i32_b64 s24, s[8:9]
	s_bcnt1_i32_b64 s8, s[10:11]
	s_add_i32 s24, s24, s8
	v_cmp_ge_i32_e64 s[8:9], s6, v163
	v_cmp_ge_i32_e64 s[10:11], s6, v52
	s_bcnt1_i32_b64 s8, s[8:9]
	s_bcnt1_i32_b64 s10, s[10:11]
	s_add_i32 s24, s24, s8
	s_add_i32 s24, s24, s10
	s_lshl_b32 s6, s24, 2
	s_add_i32 s6, s6, 0x1e800
	v_mov_b32_e32 v52, s6
	ds_read_b32 v53, v52
	ds_read_b32 v162, v52 offset:1040
	ds_read_b32 v163, v52 offset:2080
	ds_read_b32 v52, v52 offset:2084
	s_waitcnt lgkmcnt(0)
	v_readfirstlane_b32 s6, v163
	v_readfirstlane_b32 s7, v52
	v_readfirstlane_b32 s8, v53
	s_sub_i32 s7, s7, s6
	s_cmp_gt_u32 s7, 2
	s_cbranch_scc1 .Lopt24_m20_orig
	s_lshl_b32 s6, s6, 3
	s_sub_i32 s6, s23, s6
	s_and_b32 s25, s6, 7
	s_lshr_b32 s6, s6, 3
	s_add_i32 s8, s8, s7
	s_add_i32 s8, s8, -1
	s_add_i32 s7, s7, -1
	s_lshr_b32 s8, s8, s7
	s_mul_i32 s26, s6, s8
	s_add_i32 s8, s26, s8
	v_min_i32_e32 v163, s8, v53
	s_branch .LBB0_906
.Lopt24_m20_orig:
	s_lshl_b32 s6, s24, 2
	s_add_i32 s6, s6, 0
	s_add_i32 s7, s6, 0x1f020
	v_mov_b32_e32 v52, s7
	ds_read2_b32 v[52:53], v52 offset1:1
	s_add_i32 s11, s6, 0x1e800
	s_add_i32 s6, s6, 0x1ec10
	s_waitcnt lgkmcnt(0)
	v_readfirstlane_b32 s7, v52
	v_mov_b32_e32 v52, s11
	ds_read_b32 v52, v52
	v_readfirstlane_b32 s8, v53
	s_sub_i32 s8, s8, s7
	s_lshl_b32 s7, s7, 3
	s_sub_i32 s7, s23, s7
	s_ashr_i32 s9, s7, 31
	v_mov_b32_e32 v53, s6
	s_lshr_b32 s9, s9, 29
	ds_read_b32 v162, v53
	s_waitcnt lgkmcnt(1)
	v_readfirstlane_b32 s6, v52
	s_add_i32 s9, s7, s9
	s_add_i32 s6, s6, s8
	s_ashr_i32 s10, s9, 3
	s_and_b32 s9, s9, -8
	s_add_i32 s6, s6, -1
	s_sub_i32 s25, s7, s9
	s_xor_b32 s7, s6, s8
	s_abs_i32 s8, s8
	v_cvt_f32_u32_e32 v53, s8
	s_sub_i32 s9, 0, s8
	s_abs_i32 s6, s6
	s_ashr_i32 s7, s7, 31
	v_rcp_iflag_f32_e32 v53, v53
	s_nop 0
	v_mul_f32_e32 v53, 0x4f7ffffe, v53
	v_cvt_u32_f32_e32 v53, v53
	s_nop 0
	v_readfirstlane_b32 s11, v53
	s_mul_i32 s9, s9, s11
	s_mul_hi_u32 s9, s11, s9
	s_add_i32 s11, s11, s9
	s_mul_hi_u32 s9, s6, s11
	s_mul_i32 s11, s9, s8
	s_sub_i32 s6, s6, s11
	s_add_i32 s11, s9, 1
	s_sub_i32 s26, s6, s8
	s_cmp_ge_u32 s6, s8
	s_cselect_b32 s9, s11, s9
	s_cselect_b32 s6, s26, s6
	s_add_i32 s11, s9, 1
	s_cmp_ge_u32 s6, s8
	s_cselect_b32 s6, s11, s9
	s_xor_b32 s6, s6, s7
	s_sub_i32 s6, s6, s7
	s_mul_i32 s26, s10, s6
	s_add_i32 s6, s26, s6
	v_min_i32_e32 v163, s6, v52
.LBB0_906:
	s_waitcnt lgkmcnt(0)
	v_mov_b32_e32 v52, v244
	v_mov_b32_e32 v53, 0
	s_waitcnt vmcnt(7)
	v_cvt_pk_bf16_f32 v4, v4, v5
	v_mbcnt_lo_u32_b32 v53, -1, v53
	v_mbcnt_hi_u32_b32 v53, -1, v53
	s_waitcnt lgkmcnt(0)
	v_readfirstlane_b32 s6, v52
	v_cvt_pk_bf16_f32 v5, v6, v7
	s_waitcnt vmcnt(6)
	v_cvt_pk_bf16_f32 v0, v0, v1
	v_lshl_or_b32 v62, s6, 6, v53
	v_cvt_pk_bf16_f32 v1, v2, v3
	v_lshrrev_b32_e32 v53, 3, v62
	v_lshlrev_b32_e32 v54, 4, v62
	v_and_b32_e32 v68, 0x70, v54
	v_mul_lo_u32 v69, v53, s20
	v_ashrrev_i32_e32 v52, 5, v62
	v_add3_u32 v53, 0, v68, v69
	ds_write_b128 v53, v[32:35]
	ds_write_b128 v53, v[36:39] offset:9216
	ds_write_b128 v53, v[40:43] offset:18432
	s_waitcnt vmcnt(5)
	ds_write_b128 v53, v[44:47] offset:27648
	s_waitcnt vmcnt(4)
	ds_write_b128 v53, v[48:51] offset:36864
	v_lshrrev_b32_e32 v34, 1, v52
	v_bfe_u32 v32, v62, 2, 3
	v_and_b32_e32 v33, 3, v52
	v_and_b32_e32 v34, 4, v34
	v_bitop3_b32 v32, v34, v32, v33 bitop3:0x36
	v_lshlrev_b32_e32 v33, 2, v62
	v_and_b32_e32 v67, 12, v33
	v_lshlrev_b32_e32 v70, 1, v67
	v_lshl_or_b32 v130, v32, 5, v70
	v_lshlrev_b32_e32 v131, 8, v52
	v_add3_u32 v6, s21, v130, v131
	ds_write2st64_b64 v6, v[4:5], v[0:1] offset1:8
	s_waitcnt vmcnt(5)
	v_cvt_pk_bf16_f32 v0, v12, v13
	v_cvt_pk_bf16_f32 v1, v14, v15
	s_waitcnt vmcnt(4)
	v_cvt_pk_bf16_f32 v2, v8, v9
	v_cvt_pk_bf16_f32 v3, v10, v11
	ds_write2st64_b64 v6, v[0:1], v[2:3] offset0:16 offset1:24
	v_sub_u32_e32 v0, v156, v143
	v_xad_u32 v2, s14, -1, v0
	v_add_u32_e32 v1, s14, v141
	v_min_i32_e32 v0, 0, v2
	v_add_u32_e32 v3, v1, v143
	v_add_u32_e32 v0, v0, v3
	v_ashrrev_i32_e32 v1, 31, v0
	v_lshlrev_b64 v[0:1], 9, v[0:1]
	v_lshl_add_u64 v[52:53], v[134:135], 0, v[0:1]
	v_min_i32_e32 v0, 64, v2
	v_add_u32_e32 v0, v0, v3
	v_ashrrev_i32_e32 v1, 31, v0
	v_lshlrev_b64 v[0:1], 9, v[0:1]
	v_lshl_add_u64 v[54:55], v[134:135], 0, v[0:1]
	v_min_i32_e32 v0, 0x80, v2
	v_add_u32_e32 v0, v0, v3
	v_ashrrev_i32_e32 v1, 31, v0
	v_lshlrev_b64 v[0:1], 9, v[0:1]
	v_lshl_add_u64 v[56:57], v[134:135], 0, v[0:1]
	v_min_i32_e32 v0, 0xc0, v2
	v_add_u32_e32 v0, v0, v3
	v_ashrrev_i32_e32 v1, 31, v0
	v_lshlrev_b64 v[0:1], 9, v[0:1]
	v_lshl_add_u64 v[58:59], v[134:135], 0, v[0:1]
	v_min_i32_e32 v0, 0x100, v2
	v_add_u32_e32 v0, v0, v3
	v_ashrrev_i32_e32 v1, 31, v0
	v_lshlrev_b64 v[0:1], 9, v[0:1]
	v_lshl_add_u64 v[60:61], v[134:135], 0, v[0:1]
	v_lshrrev_b32_e32 v1, 2, v62
	v_bfe_u32 v65, v62, 2, 2
	v_and_b32_e32 v1, 4, v1
	v_bfe_u32 v66, v62, 6, 1
	v_lshrrev_b32_e32 v0, 1, v62
	v_or_b32_e32 v2, v1, v65
	v_and_b32_e32 v71, 24, v0
	v_lshlrev_b32_e32 v3, 6, v66
	v_lshlrev_b32_e32 v2, 4, v2
	s_cmpk_lt_i32 s13, 0x100
	v_readlane_b32 s44, v253, 4
	v_or_b32_e32 v0, v71, v65
	v_xor_b32_e32 v2, v2, v3
	s_cselect_b32 s6, s13, 0
	v_readlane_b32 s50, v253, 10
	v_readlane_b32 s51, v253, 11
	v_readlane_b32 s56, v253, 16
	v_readlane_b32 s57, v253, 17
	v_or_b32_e32 v2, v2, v67
	v_lshlrev_b32_e32 v72, 8, v0
	v_lshlrev_b32_e32 v0, 2, v66
	s_cselect_b32 s9, s51, s57
	s_cselect_b32 s8, s50, s56
	s_ashr_i32 s7, s6, 31
	v_lshlrev_b32_e32 v192, 1, v2
	v_or_b32_e32 v2, 1, v0
	s_lshl_b64 s[6:7], s[6:7], 20
	v_bitop3_b32 v2, v1, v2, v65 bitop3:0x36
	s_add_u32 s8, s8, s6
	v_lshl_or_b32 v196, v2, 5, v70
	v_or_b32_e32 v2, 2, v0
	v_or_b32_e32 v0, 3, v0
	s_addc_u32 s9, s9, s7
	s_lshl_b32 s6, s15, 7
	v_bitop3_b32 v0, v1, v0, v65 bitop3:0x36
	s_ashr_i32 s7, s6, 31
	v_bitop3_b32 v2, v1, v2, v65 bitop3:0x36
	v_lshl_or_b32 v200, v0, 5, v70
	v_lshl_add_u64 v[0:1], s[8:9], 0, v[144:145]
	s_lshl_b64 s[10:11], s[6:7], 2
	v_lshl_add_u64 v[0:1], v[0:1], 0, s[10:11]
	v_lshl_add_u64 v[0:1], v[0:1], 0, v[132:133]
	v_mov_b32_e32 v149, v133
	v_lshl_add_u64 v[0:1], v[0:1], 0, v[148:149]
	v_mov_b32_e32 v151, v133
	v_lshl_add_u64 v[0:1], v[0:1], 0, v[150:151]
	v_lshl_or_b32 v197, v2, 5, v70
	v_add_co_u32_e32 v2, vcc, s16, v0
	global_load_dwordx4 v[32:35], v[52:53], off offset:128
	global_load_dwordx4 v[36:39], v[54:55], off offset:128
	v_addc_co_u32_e32 v3, vcc, 0, v1, vcc
	global_load_dwordx4 v[40:43], v[56:57], off offset:128
	global_load_dwordx4 v[44:47], v[58:59], off offset:128
	global_load_dwordx4 v[48:51], v[60:61], off offset:128
	s_waitcnt lgkmcnt(0)
	s_barrier
	global_load_dwordx4 v[12:15], v[0:1], off
	global_load_dwordx4 v[8:11], v[2:3], off
	v_add_co_u32_e32 v2, vcc, s17, v0
	v_ashrrev_i32_e32 v63, 7, v62
	s_nop 0
	v_addc_co_u32_e32 v3, vcc, 0, v1, vcc
	v_add_co_u32_e32 v0, vcc, s18, v0
	v_and_b32_e32 v64, 15, v62
	s_nop 0
	v_addc_co_u32_e32 v1, vcc, 0, v1, vcc
	global_load_dwordx4 v[4:7], v[2:3], off
	s_nop 0
	global_load_dwordx4 v[0:3], v[0:1], off
	v_add_u32_e32 v62, s21, v72
	v_add_u32_e32 v81, v62, v192
	v_add_u32_e32 v83, v62, v196
	v_add_u32_e32 v79, v62, v197
	v_add_u32_e32 v100, v62, v200
	v_mul_lo_u32 v62, v63, s19
	v_add_u32_e32 v193, 0, v72
	v_or_b32_e32 v62, v62, v64
	v_add_u32_e32 v67, 0x16c00, v193
	v_lshlrev_b32_e32 v63, 1, v71
	v_mul_lo_u32 v62, v62, s20
	v_add_u32_e32 v82, v67, v192
	v_add_u32_e32 v84, v67, v196
	v_add_u32_e32 v80, v67, v197
	v_add_u32_e32 v101, v67, v200
	v_add3_u32 v62, 0, v63, v62
	ds_read_b64_tr_b16 v[102:103], v81
	ds_read_b64_tr_b16 v[104:105], v82
	ds_read_b64_tr_b16 v[106:107], v83
	ds_read_b64_tr_b16 v[108:109], v84
	ds_read_b128 v[64:67], v62
	ds_read_b64_tr_b16 v[110:111], v79
	ds_read_b64_tr_b16 v[112:113], v80
	ds_read_b128 v[114:117], v62 offset:2304
	ds_read_b64_tr_b16 v[122:123], v100
	ds_read_b64_tr_b16 v[124:125], v101
	s_waitcnt lgkmcnt(5)
	v_mfma_f32_16x16x32_bf16 v[118:121], v[102:105], v[64:67], 0
	v_add3_u32 v63, 0, v131, v130
	v_or_b32_e32 v201, 0x2000, v72
	v_add_u32_e32 v70, 0x18c00, v193
	v_mfma_f32_16x16x32_bf16 v[126:129], v[106:109], v[64:67], 0
	v_add3_u32 v86, 0, v69, v68
	v_add_u32_e32 v68, s22, v72
	ds_read_b128 v[180:183], v62 offset:4608
	ds_read_b128 v[184:187], v62 offset:6912
	s_waitcnt lgkmcnt(5)
	v_mfma_f32_16x16x32_bf16 v[152:155], v[110:113], v[64:67], 0
	v_add_u32_e32 v98, 0x1b800, v63
	v_add_u32_e32 v95, 0x1c800, v63
	v_add_u32_e32 v92, 0x1d800, v63
	s_waitcnt lgkmcnt(2)
	v_mfma_f32_16x16x32_bf16 v[164:167], v[122:125], v[64:67], 0
	v_add_u32_e32 v64, 0x1ac00, v193
	v_add_u32_e32 v78, v64, v192
	v_add_u32_e32 v75, v64, v196
	v_add_u32_e32 v73, v64, v197
	v_add_u32_e32 v72, v64, v200
	v_add_u32_e32 v64, 0x1cc00, v193
	v_add3_u32 v91, s21, v192, v201
	v_add_u32_e32 v93, v70, v192
	v_add3_u32 v89, s21, v196, v201
	v_add_u32_e32 v90, v70, v196
	v_add3_u32 v85, s21, v197, v201
	v_add_u32_e32 v94, v70, v197
	v_add3_u32 v96, s21, v200, v201
	v_add_u32_e32 v97, v70, v200
	v_add_u32_e32 v77, v68, v192
	v_add_u32_e32 v74, v68, v196
	v_mfma_f32_16x16x32_bf16 v[168:171], v[102:105], v[114:117], 0
	v_add_u32_e32 v76, v68, v197
	v_add_u32_e32 v71, v68, v200
	v_add_u32_e32 v241, 0x17800, v63
	v_mfma_f32_16x16x32_bf16 v[172:175], v[106:109], v[114:117], 0
	v_add_u32_e32 v242, 0x18800, v63
	v_add_u32_e32 v243, 0x19800, v63
	v_add3_u32 v68, s22, v192, v201
	v_mfma_f32_16x16x32_bf16 v[176:179], v[110:113], v[114:117], 0
	v_add_u32_e32 v70, v64, v192
	v_add3_u32 v67, s22, v196, v201
	v_add_u32_e32 v69, v64, v196
	v_mfma_f32_16x16x32_bf16 v[114:117], v[122:125], v[114:117], 0
	v_add3_u32 v65, s22, v197, v201
	v_add_u32_e32 v66, v64, v197
	v_add3_u32 v63, s22, v200, v201
	v_add_u32_e32 v64, v64, v200
	ds_read_b128 v[200:203], v62 offset:9216
	v_add3_u32 v99, s22, v131, v130
	v_add_u32_e32 v87, 0x12000, v86
	v_add_u32_e32 v88, 0x14400, v86
	s_waitcnt vmcnt(12)
	v_cvt_pk_bf16_f32 v28, v28, v29
	v_cvt_pk_bf16_f32 v29, v30, v31
	s_waitcnt vmcnt(11)
	v_cvt_pk_bf16_f32 v24, v24, v25
	v_cvt_pk_bf16_f32 v25, v26, v27
	v_readlane_b32 s45, v253, 5
	v_readlane_b32 s46, v253, 6
	v_readlane_b32 s47, v253, 7
	v_readlane_b32 s48, v253, 8
	v_readlane_b32 s49, v253, 9
	v_readlane_b32 s52, v253, 12
	v_readlane_b32 s53, v253, 13
	v_readlane_b32 s54, v253, 14
	v_readlane_b32 s55, v253, 15
	v_readlane_b32 s58, v253, 18
	v_readlane_b32 s59, v253, 19
	v_add3_u32 v240, s21, v131, v130
	s_waitcnt lgkmcnt(2)
	v_mfma_f32_16x16x32_bf16 v[188:191], v[102:105], v[180:183], 0
	ds_write_b64 v99, v[28:29]
	ds_write_b64 v98, v[24:25]
	v_mfma_f32_16x16x32_bf16 v[192:195], v[106:109], v[180:183], 0
	v_mfma_f32_16x16x32_bf16 v[196:199], v[110:113], v[180:183], 0
	v_mfma_f32_16x16x32_bf16 v[180:183], v[122:125], v[180:183], 0
	ds_read_b128 v[208:211], v62 offset:64
	ds_read_b128 v[212:215], v62 offset:2368
	s_waitcnt vmcnt(9)
	v_cvt_pk_bf16_f32 v16, v16, v17
	v_cvt_pk_bf16_f32 v17, v18, v19
	s_waitcnt lgkmcnt(5)
	v_mfma_f32_16x16x32_bf16 v[24:27], v[102:105], v[184:187], 0
	ds_read_b128 v[216:219], v62 offset:4672
	v_cvt_pk_bf16_f32 v130, v20, v21
	v_cvt_pk_bf16_f32 v131, v22, v23
	v_mfma_f32_16x16x32_bf16 v[28:31], v[106:109], v[184:187], 0
	ds_write_b64 v92, v[16:17]
	ds_write_b64 v95, v[130:131]
	s_waitcnt lgkmcnt(7)
	v_mfma_f32_16x16x32_bf16 v[102:105], v[102:105], v[200:203], 0
	v_mfma_f32_16x16x32_bf16 v[106:109], v[106:109], v[200:203], 0
	v_mfma_f32_16x16x32_bf16 v[20:23], v[110:113], v[200:203], 0
	v_mfma_f32_16x16x32_bf16 v[16:19], v[122:125], v[200:203], 0
	v_mfma_f32_16x16x32_bf16 v[204:207], v[110:113], v[184:187], 0
	v_mfma_f32_16x16x32_bf16 v[184:187], v[122:125], v[184:187], 0
	ds_read_b64_tr_b16 v[110:111], v91
	ds_read_b64_tr_b16 v[112:113], v93
	ds_read_b64_tr_b16 v[122:123], v89
	ds_read_b64_tr_b16 v[124:125], v90
	ds_read_b64_tr_b16 v[200:201], v85
	ds_read_b64_tr_b16 v[202:203], v94
	ds_read_b64_tr_b16 v[220:221], v96
	ds_read_b64_tr_b16 v[222:223], v97
	s_waitcnt lgkmcnt(6)
	v_mfma_f32_16x16x32_bf16 v[118:121], v[110:113], v[208:211], v[118:121]
	s_waitcnt lgkmcnt(4)
	v_mfma_f32_16x16x32_bf16 v[126:129], v[122:125], v[208:211], v[126:129]
	s_waitcnt lgkmcnt(2)
	v_mfma_f32_16x16x32_bf16 v[152:155], v[200:203], v[208:211], v[152:155]
	s_waitcnt lgkmcnt(0)
	v_mfma_f32_16x16x32_bf16 v[164:167], v[220:223], v[208:211], v[164:167]
	v_mfma_f32_16x16x32_bf16 v[168:171], v[110:113], v[212:215], v[168:171]
	v_mfma_f32_16x16x32_bf16 v[172:175], v[122:125], v[212:215], v[172:175]
	v_mfma_f32_16x16x32_bf16 v[176:179], v[200:203], v[212:215], v[176:179]
	v_mfma_f32_16x16x32_bf16 v[114:117], v[220:223], v[212:215], v[114:117]
	ds_read_b128 v[208:211], v62 offset:6976
	ds_read_b128 v[212:215], v62 offset:9280
	s_waitcnt vmcnt(8)
	ds_write_b128 v86, v[32:35] offset:46080
	s_waitcnt vmcnt(7)
	ds_write_b128 v86, v[36:39] offset:55296
	v_mfma_f32_16x16x32_bf16 v[32:35], v[220:223], v[216:219], v[180:183]
	v_mfma_f32_16x16x32_bf16 v[188:191], v[110:113], v[216:219], v[188:191]
	v_mfma_f32_16x16x32_bf16 v[192:195], v[122:125], v[216:219], v[192:195]
	v_mfma_f32_16x16x32_bf16 v[196:199], v[200:203], v[216:219], v[196:199]
	s_waitcnt vmcnt(6)
	ds_write_b128 v86, v[40:43] offset:64512
	s_waitcnt vmcnt(5)
	ds_write_b128 v87, v[44:47]
	s_waitcnt vmcnt(4)
	ds_write_b128 v88, v[48:51]
	s_waitcnt lgkmcnt(6)
	v_mfma_f32_16x16x32_bf16 v[36:39], v[110:113], v[208:211], v[24:27]
	v_mfma_f32_16x16x32_bf16 v[180:183], v[122:125], v[208:211], v[28:31]
	v_mfma_f32_16x16x32_bf16 v[204:207], v[200:203], v[208:211], v[204:207]
	v_mfma_f32_16x16x32_bf16 v[184:187], v[220:223], v[208:211], v[184:187]
	s_waitcnt lgkmcnt(5)
	v_mfma_f32_16x16x32_bf16 v[102:105], v[110:113], v[212:215], v[102:105]
	v_mfma_f32_16x16x32_bf16 v[110:113], v[200:203], v[212:215], v[20:23]
	global_load_dwordx4 v[40:43], v[52:53], off offset:256
	global_load_dwordx4 v[44:47], v[54:55], off offset:256
	global_load_dwordx4 v[48:51], v[56:57], off offset:256
	global_load_dwordx4 v[200:203], v[58:59], off offset:256
	global_load_dwordx4 v[208:211], v[60:61], off offset:256
	v_mfma_f32_16x16x32_bf16 v[106:109], v[122:125], v[212:215], v[106:109]
	v_mfma_f32_16x16x32_bf16 v[122:125], v[220:223], v[212:215], v[16:19]
	s_waitcnt lgkmcnt(0)
	s_barrier
	ds_read_b64_tr_b16 v[212:213], v77
	ds_read_b64_tr_b16 v[214:215], v78
	ds_read_b128 v[16:19], v62 offset:46080
	ds_read_b64_tr_b16 v[216:217], v74
	ds_read_b64_tr_b16 v[218:219], v75
	ds_read_b64_tr_b16 v[220:221], v76
	ds_read_b128 v[20:23], v62 offset:48384
	ds_read_b128 v[224:227], v62 offset:55296
	ds_read_b64_tr_b16 v[222:223], v73
	ds_read_b64_tr_b16 v[228:229], v71
	ds_read_b64_tr_b16 v[230:231], v72
	s_waitcnt lgkmcnt(8)
	v_mfma_f32_16x16x32_bf16 v[118:121], v[212:215], v[16:19], v[118:121]
	ds_read_b128 v[232:235], v62 offset:50688
	s_waitcnt vmcnt(8)
	v_cvt_pk_bf16_f32 v12, v12, v13
	v_cvt_pk_bf16_f32 v13, v14, v15
	s_waitcnt lgkmcnt(7)
	v_mfma_f32_16x16x32_bf16 v[126:129], v[216:219], v[16:19], v[126:129]
	s_waitcnt vmcnt(7)
	v_cvt_pk_bf16_f32 v8, v8, v9
	v_cvt_pk_bf16_f32 v9, v10, v11
	s_waitcnt lgkmcnt(3)
	v_mfma_f32_16x16x32_bf16 v[152:155], v[220:223], v[16:19], v[152:155]
	s_waitcnt lgkmcnt(1)
	v_mfma_f32_16x16x32_bf16 v[164:167], v[228:231], v[16:19], v[164:167]
	v_lshl_add_u64 v[16:17], s[8:9], 0, v[146:147]
	v_lshl_add_u64 v[16:17], v[16:17], 0, s[10:11]
	v_lshl_add_u64 v[16:17], v[16:17], 0, v[132:133]
	v_lshl_add_u64 v[16:17], v[16:17], 0, v[148:149]
	v_lshl_add_u64 v[16:17], v[16:17], 0, v[150:151]
	v_add_co_u32_e32 v18, vcc, s16, v16
	v_mfma_f32_16x16x32_bf16 v[168:171], v[212:215], v[20:23], v[168:171]
	s_nop 0
	v_addc_co_u32_e32 v19, vcc, 0, v17, vcc
	global_load_dwordx4 v[28:31], v[16:17], off
	global_load_dwordx4 v[24:27], v[18:19], off
	v_add_co_u32_e32 v18, vcc, s17, v16
	v_mfma_f32_16x16x32_bf16 v[172:175], v[216:219], v[20:23], v[172:175]
	s_nop 0
	v_addc_co_u32_e32 v19, vcc, 0, v17, vcc
	v_add_co_u32_e32 v16, vcc, s18, v16
	v_mfma_f32_16x16x32_bf16 v[176:179], v[220:223], v[20:23], v[176:179]
	s_nop 0
	v_addc_co_u32_e32 v17, vcc, 0, v17, vcc
	ds_read_b128 v[236:239], v62 offset:52992
	v_mfma_f32_16x16x32_bf16 v[114:117], v[228:231], v[20:23], v[114:117]
	global_load_dwordx4 v[20:23], v[18:19], off
	s_nop 0
	global_load_dwordx4 v[16:19], v[16:17], off
	ds_write_b64 v240, v[12:13]
	ds_write_b64 v241, v[8:9]
	s_waitcnt lgkmcnt(3)
	v_mfma_f32_16x16x32_bf16 v[32:35], v[228:231], v[232:235], v[32:35]
	v_mfma_f32_16x16x32_bf16 v[188:191], v[212:215], v[232:235], v[188:191]
	v_mfma_f32_16x16x32_bf16 v[192:195], v[216:219], v[232:235], v[192:195]
	v_mfma_f32_16x16x32_bf16 v[196:199], v[220:223], v[232:235], v[196:199]
	s_waitcnt lgkmcnt(2)
	v_mfma_f32_16x16x32_bf16 v[8:11], v[212:215], v[236:239], v[36:39]
	s_waitcnt vmcnt(9)
	v_cvt_pk_bf16_f32 v0, v0, v1
	v_cvt_pk_bf16_f32 v1, v2, v3
	v_cvt_pk_bf16_f32 v130, v4, v5
	v_mfma_f32_16x16x32_bf16 v[12:15], v[216:219], v[236:239], v[180:183]
	v_cvt_pk_bf16_f32 v131, v6, v7
	v_mfma_f32_16x16x32_bf16 v[36:39], v[220:223], v[236:239], v[204:207]
	v_mfma_f32_16x16x32_bf16 v[180:183], v[228:231], v[236:239], v[184:187]
	s_nop 2
	ds_read_b128 v[184:187], v62 offset:46144
	ds_read_b128 v[204:207], v62 offset:48448
	v_mfma_f32_16x16x32_bf16 v[102:105], v[212:215], v[224:227], v[102:105]
	ds_read_b128 v[212:215], v62 offset:50752
	ds_write_b64 v243, v[0:1]
	ds_write_b64 v242, v[130:131]
	v_mfma_f32_16x16x32_bf16 v[106:109], v[216:219], v[224:227], v[106:109]
	v_mfma_f32_16x16x32_bf16 v[4:7], v[220:223], v[224:227], v[110:113]
	v_mfma_f32_16x16x32_bf16 v[0:3], v[228:231], v[224:227], v[122:125]
	s_nop 1
	ds_read_b64_tr_b16 v[110:111], v68
	ds_read_b64_tr_b16 v[112:113], v70
	ds_read_b64_tr_b16 v[122:123], v67
	ds_read_b64_tr_b16 v[124:125], v69
	ds_read_b64_tr_b16 v[216:217], v65
	ds_read_b64_tr_b16 v[218:219], v66
	ds_read_b64_tr_b16 v[220:221], v63
	ds_read_b64_tr_b16 v[222:223], v64
	s_waitcnt lgkmcnt(6)
	v_mfma_f32_16x16x32_bf16 v[118:121], v[110:113], v[184:187], v[118:121]
	s_waitcnt lgkmcnt(4)
	v_mfma_f32_16x16x32_bf16 v[126:129], v[122:125], v[184:187], v[126:129]
	s_waitcnt lgkmcnt(2)
	v_mfma_f32_16x16x32_bf16 v[152:155], v[216:219], v[184:187], v[152:155]
	s_waitcnt lgkmcnt(0)
	v_mfma_f32_16x16x32_bf16 v[164:167], v[220:223], v[184:187], v[164:167]
	v_mfma_f32_16x16x32_bf16 v[168:171], v[110:113], v[204:207], v[168:171]
	v_mfma_f32_16x16x32_bf16 v[172:175], v[122:125], v[204:207], v[172:175]
	v_mfma_f32_16x16x32_bf16 v[176:179], v[216:219], v[204:207], v[176:179]
	v_mfma_f32_16x16x32_bf16 v[114:117], v[220:223], v[204:207], v[114:117]
	v_mfma_f32_16x16x32_bf16 v[184:187], v[110:113], v[212:215], v[188:191]
	v_mfma_f32_16x16x32_bf16 v[188:191], v[122:125], v[212:215], v[192:195]
	v_mfma_f32_16x16x32_bf16 v[192:195], v[216:219], v[212:215], v[196:199]
	s_nop 2
	ds_read_b128 v[196:199], v62 offset:53056
	ds_read_b128 v[204:207], v62 offset:55360
	s_waitcnt vmcnt(8)
	ds_write_b128 v86, v[40:43]
	s_waitcnt vmcnt(7)
	ds_write_b128 v86, v[44:47] offset:9216
	v_mfma_f32_16x16x32_bf16 v[32:35], v[220:223], v[212:215], v[32:35]
	s_waitcnt lgkmcnt(3)
	v_mfma_f32_16x16x32_bf16 v[40:43], v[110:113], v[196:199], v[8:11]
	v_mfma_f32_16x16x32_bf16 v[44:47], v[122:125], v[196:199], v[12:15]
	v_mfma_f32_16x16x32_bf16 v[36:39], v[216:219], v[196:199], v[36:39]
	v_mfma_f32_16x16x32_bf16 v[180:183], v[220:223], v[196:199], v[180:183]
	s_waitcnt lgkmcnt(2)
	v_mfma_f32_16x16x32_bf16 v[102:105], v[110:113], v[204:207], v[102:105]
	v_mfma_f32_16x16x32_bf16 v[106:109], v[122:125], v[204:207], v[106:109]
	global_load_dwordx4 v[110:113], v[52:53], off offset:384
	s_nop 0
	global_load_dwordx4 v[52:55], v[54:55], off offset:384
	s_nop 0
	global_load_dwordx4 v[122:125], v[56:57], off offset:384
	s_nop 0
	global_load_dwordx4 v[56:59], v[58:59], off offset:384
	s_nop 0
	global_load_dwordx4 v[196:199], v[60:61], off offset:384
	s_waitcnt vmcnt(11)
	ds_write_b128 v86, v[48:51] offset:18432
	s_waitcnt vmcnt(10)
	ds_write_b128 v86, v[200:203] offset:27648
	s_waitcnt vmcnt(9)
	ds_write_b128 v86, v[208:211] offset:36864
	v_mfma_f32_16x16x32_bf16 v[48:51], v[220:223], v[204:207], v[0:3]
	v_mfma_f32_16x16x32_bf16 v[212:215], v[216:219], v[204:207], v[4:7]
	s_waitcnt lgkmcnt(0)
	s_barrier
	ds_read_b64_tr_b16 v[200:201], v81
	ds_read_b64_tr_b16 v[202:203], v82
	ds_read_b64_tr_b16 v[204:205], v83
	ds_read_b64_tr_b16 v[206:207], v84
	ds_read_b128 v[0:3], v62
	ds_read_b64_tr_b16 v[208:209], v79
	ds_read_b64_tr_b16 v[210:211], v80
	ds_read_b128 v[4:7], v62 offset:2304
	s_cmpk_lt_i32 s24, 0x100
	s_cselect_b32 s8, s24, 0
	s_waitcnt lgkmcnt(3)
	v_mfma_f32_16x16x32_bf16 v[80:83], v[200:203], v[0:3], v[118:121]
	s_nop 2
	ds_read_b64_tr_b16 v[118:119], v100
	ds_read_b64_tr_b16 v[120:121], v101
	s_cselect_b32 s10, s51, s57
	s_cselect_b32 s11, s50, s56
	s_ashr_i32 s9, s8, 31
	s_lshl_b64 s[8:9], s[8:9], 20
	s_add_u32 s8, s11, s8
	s_addc_u32 s9, s10, s9
	s_lshl_b32 s10, s25, 7
	s_ashr_i32 s11, s10, 31
	v_mfma_f32_16x16x32_bf16 v[126:129], v[204:207], v[0:3], v[126:129]
	s_lshl_b64 s[10:11], s[10:11], 2
	ds_read_b128 v[216:219], v62 offset:4608
	s_waitcnt vmcnt(8)
	v_cvt_pk_bf16_f32 v28, v28, v29
	s_waitcnt lgkmcnt(4)
	v_mfma_f32_16x16x32_bf16 v[152:155], v[208:211], v[0:3], v[152:155]
	v_cvt_pk_bf16_f32 v29, v30, v31
	s_waitcnt vmcnt(7)
	v_cvt_pk_bf16_f32 v24, v24, v25
	v_cvt_pk_bf16_f32 v25, v26, v27
	s_waitcnt lgkmcnt(1)
	v_mfma_f32_16x16x32_bf16 v[164:167], v[118:121], v[0:3], v[164:167]
	v_lshl_add_u64 v[0:1], s[8:9], 0, v[136:137]
	v_lshl_add_u64 v[0:1], v[0:1], 0, s[10:11]
	v_lshl_add_u64 v[0:1], v[0:1], 0, v[132:133]
	v_lshl_add_u64 v[0:1], v[0:1], 0, v[148:149]
	v_lshl_add_u64 v[8:9], v[0:1], 0, v[150:151]
	v_add_co_u32_e32 v0, vcc, s16, v8
	v_mfma_f32_16x16x32_bf16 v[168:171], v[200:203], v[4:7], v[168:171]
	s_nop 0
	v_addc_co_u32_e32 v1, vcc, 0, v9, vcc
	v_add_co_u32_e32 v10, vcc, s17, v8
	v_mfma_f32_16x16x32_bf16 v[172:175], v[204:207], v[4:7], v[172:175]
	s_nop 0
	v_addc_co_u32_e32 v11, vcc, 0, v9, vcc
	v_mfma_f32_16x16x32_bf16 v[176:179], v[208:211], v[4:7], v[176:179]
	v_mfma_f32_16x16x32_bf16 v[114:117], v[118:121], v[4:7], v[114:117]
	global_load_dwordx4 v[4:7], v[8:9], off
	s_nop 0
	global_load_dwordx4 v[0:3], v[0:1], off
	v_add_co_u32_e32 v8, vcc, s18, v8
	ds_read_b128 v[220:223], v62 offset:6912
	s_nop 0
	v_addc_co_u32_e32 v9, vcc, 0, v9, vcc
	global_load_dwordx4 v[12:15], v[10:11], off
	s_nop 0
	global_load_dwordx4 v[8:11], v[8:9], off
	ds_read_b128 v[224:227], v62 offset:9216
	s_waitcnt lgkmcnt(2)
	v_mfma_f32_16x16x32_bf16 v[32:35], v[118:121], v[216:219], v[32:35]
	ds_write_b64 v99, v[28:29]
	ds_write_b64 v98, v[24:25]
	v_mfma_f32_16x16x32_bf16 v[184:187], v[200:203], v[216:219], v[184:187]
	v_mfma_f32_16x16x32_bf16 v[188:191], v[204:207], v[216:219], v[188:191]
	v_mfma_f32_16x16x32_bf16 v[192:195], v[208:211], v[216:219], v[192:195]
	s_waitcnt lgkmcnt(3)
	v_mfma_f32_16x16x32_bf16 v[28:31], v[204:207], v[220:223], v[44:47]
	s_waitcnt vmcnt(9)
	v_cvt_pk_bf16_f32 v16, v16, v17
	v_cvt_pk_bf16_f32 v17, v18, v19
	v_cvt_pk_bf16_f32 v60, v20, v21
	s_waitcnt lgkmcnt(2)
	v_mfma_f32_16x16x32_bf16 v[44:47], v[200:203], v[224:227], v[102:105]
	ds_read_b128 v[98:101], v62 offset:64
	s_nop 1
	ds_read_b128 v[102:105], v62 offset:2368
	v_cvt_pk_bf16_f32 v61, v22, v23
	v_mfma_f32_16x16x32_bf16 v[24:27], v[200:203], v[220:223], v[40:43]
	v_mfma_f32_16x16x32_bf16 v[36:39], v[208:211], v[220:223], v[36:39]
	v_mfma_f32_16x16x32_bf16 v[40:43], v[118:121], v[220:223], v[180:183]
	v_mfma_f32_16x16x32_bf16 v[106:109], v[204:207], v[224:227], v[106:109]
	s_nop 1
	ds_read_b128 v[180:183], v62 offset:4672
	ds_write_b64 v92, v[16:17]
	ds_write_b64 v95, v[60:61]
	v_mfma_f32_16x16x32_bf16 v[20:23], v[208:211], v[224:227], v[212:215]
	v_mfma_f32_16x16x32_bf16 v[16:19], v[118:121], v[224:227], v[48:51]
	s_nop 2
	ds_read_b64_tr_b16 v[48:49], v91
	ds_read_b64_tr_b16 v[50:51], v93
	ds_read_b64_tr_b16 v[118:119], v89
	ds_read_b64_tr_b16 v[120:121], v90
	ds_read_b64_tr_b16 v[90:91], v85
	ds_read_b64_tr_b16 v[92:93], v94
	ds_read_b64_tr_b16 v[94:95], v96
	ds_read_b64_tr_b16 v[96:97], v97
	s_waitcnt lgkmcnt(6)
	v_mfma_f32_16x16x32_bf16 v[80:83], v[48:51], v[98:101], v[80:83]
	s_waitcnt lgkmcnt(4)
	v_mfma_f32_16x16x32_bf16 v[126:129], v[118:121], v[98:101], v[126:129]
	s_waitcnt lgkmcnt(2)
	v_mfma_f32_16x16x32_bf16 v[152:155], v[90:93], v[98:101], v[152:155]
	s_waitcnt lgkmcnt(0)
	v_mfma_f32_16x16x32_bf16 v[98:101], v[94:97], v[98:101], v[164:167]
	v_mfma_f32_16x16x32_bf16 v[164:167], v[48:51], v[102:105], v[168:171]
	v_mfma_f32_16x16x32_bf16 v[168:171], v[118:121], v[102:105], v[172:175]
	v_mfma_f32_16x16x32_bf16 v[172:175], v[90:93], v[102:105], v[176:179]
	v_mfma_f32_16x16x32_bf16 v[102:105], v[94:97], v[102:105], v[114:117]
	v_mfma_f32_16x16x32_bf16 v[114:117], v[48:51], v[180:183], v[184:187]
	v_mfma_f32_16x16x32_bf16 v[176:179], v[118:121], v[180:183], v[188:191]
	v_mfma_f32_16x16x32_bf16 v[184:187], v[90:93], v[180:183], v[192:195]
	s_nop 1
	ds_read_b128 v[188:191], v62 offset:6976
	ds_read_b128 v[192:195], v62 offset:9280
	s_waitcnt vmcnt(8)
	ds_write_b128 v86, v[110:113] offset:46080
	s_waitcnt vmcnt(7)
	ds_write_b128 v86, v[52:55] offset:55296
	v_mfma_f32_16x16x32_bf16 v[52:55], v[94:97], v[180:183], v[32:35]
	s_waitcnt lgkmcnt(3)
	v_mfma_f32_16x16x32_bf16 v[110:113], v[48:51], v[188:191], v[24:27]
	s_waitcnt vmcnt(6)
	ds_write_b128 v86, v[122:125] offset:64512
	s_waitcnt vmcnt(5)
	ds_write_b128 v87, v[56:59]
	s_waitcnt vmcnt(4)
	ds_write_b128 v88, v[196:199]
	v_mfma_f32_16x16x32_bf16 v[180:183], v[118:121], v[188:191], v[28:31]
	v_mfma_f32_16x16x32_bf16 v[200:203], v[90:93], v[188:191], v[36:39]
	v_mfma_f32_16x16x32_bf16 v[188:191], v[94:97], v[188:191], v[40:43]
	s_waitcnt lgkmcnt(5)
	v_mfma_f32_16x16x32_bf16 v[94:97], v[94:97], v[192:195], v[16:19]
	s_nop 2
	v_sub_u32_e32 v16, v163, v143
	v_xad_u32 v18, s26, -1, v16
	v_add_u32_e32 v17, s26, v162
	v_min_i32_e32 v16, 0, v18
	v_add_u32_e32 v19, v17, v143
	v_add_u32_e32 v16, v16, v19
	v_ashrrev_i32_e32 v17, 31, v16
	v_lshlrev_b64 v[16:17], 9, v[16:17]
	v_lshl_add_u64 v[16:17], v[134:135], 0, v[16:17]
	global_load_dwordx4 v[32:35], v[16:17], off
	v_min_i32_e32 v16, 64, v18
	v_add_u32_e32 v16, v16, v19
	v_ashrrev_i32_e32 v17, 31, v16
	v_lshlrev_b64 v[16:17], 9, v[16:17]
	v_lshl_add_u64 v[16:17], v[134:135], 0, v[16:17]
	global_load_dwordx4 v[36:39], v[16:17], off
	v_min_i32_e32 v16, 0x80, v18
	v_add_u32_e32 v16, v16, v19
	v_ashrrev_i32_e32 v17, 31, v16
	v_lshlrev_b64 v[16:17], 9, v[16:17]
	v_lshl_add_u64 v[16:17], v[134:135], 0, v[16:17]
	global_load_dwordx4 v[40:43], v[16:17], off
	v_min_i32_e32 v16, 0xc0, v18
	v_add_u32_e32 v16, v16, v19
	v_ashrrev_i32_e32 v17, 31, v16
	v_lshlrev_b64 v[16:17], 9, v[16:17]
	v_lshl_add_u64 v[16:17], v[134:135], 0, v[16:17]
	v_mfma_f32_16x16x32_bf16 v[204:207], v[48:51], v[192:195], v[44:47]
	s_nop 2
	global_load_dwordx4 v[44:47], v[16:17], off
	v_min_i32_e32 v16, 0x100, v18
	v_add_u32_e32 v16, v16, v19
	v_ashrrev_i32_e32 v17, 31, v16
	v_lshlrev_b64 v[16:17], 9, v[16:17]
	v_lshl_add_u64 v[16:17], v[134:135], 0, v[16:17]
	global_load_dwordx4 v[48:51], v[16:17], off
	v_mfma_f32_16x16x32_bf16 v[106:109], v[118:121], v[192:195], v[106:109]
	v_mfma_f32_16x16x32_bf16 v[90:93], v[90:93], v[192:195], v[20:23]
	s_waitcnt lgkmcnt(0)
	s_barrier
	ds_read_b64_tr_b16 v[56:57], v77
	ds_read_b64_tr_b16 v[58:59], v78
	ds_read_b128 v[16:19], v62 offset:46080
	ds_read_b64_tr_b16 v[84:85], v74
	ds_read_b64_tr_b16 v[86:87], v75
	ds_read_b64_tr_b16 v[74:75], v76
	ds_read_b128 v[20:23], v62 offset:48384
	ds_read_b128 v[118:121], v62 offset:55296
	ds_read_b64_tr_b16 v[76:77], v73
	s_waitcnt lgkmcnt(4)
	v_mfma_f32_16x16x32_bf16 v[122:125], v[84:87], v[16:19], v[126:129]
	s_nop 2
	ds_read_b64_tr_b16 v[126:127], v71
	ds_read_b64_tr_b16 v[128:129], v72
	ds_read_b128 v[192:195], v62 offset:50688
	v_mfma_f32_16x16x32_bf16 v[78:81], v[56:59], v[16:19], v[80:83]
	s_waitcnt lgkmcnt(3)
	v_mfma_f32_16x16x32_bf16 v[152:155], v[74:77], v[16:19], v[152:155]
	s_waitcnt lgkmcnt(1)
	v_mfma_f32_16x16x32_bf16 v[98:101], v[126:129], v[16:19], v[98:101]
	v_lshl_add_u64 v[16:17], s[8:9], 0, v[138:139]
	v_lshl_add_u64 v[16:17], v[16:17], 0, s[10:11]
	v_lshl_add_u64 v[16:17], v[16:17], 0, v[132:133]
	v_lshl_add_u64 v[16:17], v[16:17], 0, v[148:149]
	v_lshl_add_u64 v[16:17], v[16:17], 0, v[150:151]
	v_add_co_u32_e32 v18, vcc, s16, v16
	v_mfma_f32_16x16x32_bf16 v[164:167], v[56:59], v[20:23], v[164:167]
	s_nop 0
	v_addc_co_u32_e32 v19, vcc, 0, v17, vcc
	global_load_dwordx4 v[28:31], v[16:17], off
	global_load_dwordx4 v[24:27], v[18:19], off
	v_add_co_u32_e32 v18, vcc, s17, v16
	v_mfma_f32_16x16x32_bf16 v[168:171], v[84:87], v[20:23], v[168:171]
	s_nop 0
	v_addc_co_u32_e32 v19, vcc, 0, v17, vcc
	v_add_co_u32_e32 v16, vcc, s18, v16
	v_mfma_f32_16x16x32_bf16 v[172:175], v[74:77], v[20:23], v[172:175]
	s_nop 0
	v_addc_co_u32_e32 v17, vcc, 0, v17, vcc
	v_mfma_f32_16x16x32_bf16 v[196:199], v[126:129], v[20:23], v[102:105]
	s_nop 2
	ds_read_b128 v[102:105], v62 offset:52992
	global_load_dwordx4 v[20:23], v[18:19], off
	s_nop 0
	global_load_dwordx4 v[16:19], v[16:17], off
	s_waitcnt lgkmcnt(1)
	v_mfma_f32_16x16x32_bf16 v[52:55], v[126:129], v[192:195], v[52:55]
	v_mfma_f32_16x16x32_bf16 v[208:211], v[56:59], v[192:195], v[114:117]
	v_mfma_f32_16x16x32_bf16 v[176:179], v[84:87], v[192:195], v[176:179]
	v_mfma_f32_16x16x32_bf16 v[184:187], v[74:77], v[192:195], v[184:187]
	s_waitcnt lgkmcnt(0)
	v_mfma_f32_16x16x32_bf16 v[192:195], v[56:59], v[102:105], v[110:113]
	v_mfma_f32_16x16x32_bf16 v[180:183], v[84:87], v[102:105], v[180:183]
	v_mfma_f32_16x16x32_bf16 v[200:203], v[74:77], v[102:105], v[200:203]
	v_mfma_f32_16x16x32_bf16 v[56:59], v[56:59], v[118:121], v[204:207]
	v_mfma_f32_16x16x32_bf16 v[204:207], v[84:87], v[118:121], v[106:109]
	v_mfma_f32_16x16x32_bf16 v[212:215], v[74:77], v[118:121], v[90:93]
	ds_read_b128 v[72:75], v62 offset:46144
	ds_read_b128 v[82:85], v62 offset:48448
	s_nop 0
	ds_read_b128 v[88:91], v62 offset:50752
	v_mfma_f32_16x16x32_bf16 v[188:191], v[126:129], v[102:105], v[188:191]
	v_mfma_f32_16x16x32_bf16 v[216:219], v[126:129], v[118:121], v[94:97]
	ds_read_b64_tr_b16 v[220:221], v68
	ds_read_b64_tr_b16 v[222:223], v70
	ds_read_b64_tr_b16 v[224:225], v67
	ds_read_b64_tr_b16 v[226:227], v69
	ds_read_b64_tr_b16 v[228:229], v65
	ds_read_b64_tr_b16 v[230:231], v66
	ds_read_b64_tr_b16 v[232:233], v63
	ds_read_b64_tr_b16 v[234:235], v64
	s_waitcnt lgkmcnt(6)
	v_mfma_f32_16x16x32_bf16 v[116:119], v[220:223], v[72:75], v[78:81]
	s_waitcnt lgkmcnt(4)
	v_mfma_f32_16x16x32_bf16 v[128:131], v[224:227], v[72:75], v[122:125]
	s_waitcnt lgkmcnt(2)
	v_mfma_f32_16x16x32_bf16 v[120:123], v[228:231], v[72:75], v[152:155]
	ds_read_b128 v[64:67], v62 offset:53056
	s_nop 1
	ds_read_b128 v[152:155], v62 offset:55360
	s_waitcnt lgkmcnt(2)
	v_mfma_f32_16x16x32_bf16 v[124:127], v[232:235], v[72:75], v[98:101]
	v_mfma_f32_16x16x32_bf16 v[112:115], v[220:223], v[82:85], v[164:167]
	v_mfma_f32_16x16x32_bf16 v[108:111], v[224:227], v[82:85], v[168:171]
	v_mfma_f32_16x16x32_bf16 v[104:107], v[228:231], v[82:85], v[172:175]
	v_mfma_f32_16x16x32_bf16 v[100:103], v[232:235], v[82:85], v[196:199]
	v_mfma_f32_16x16x32_bf16 v[96:99], v[220:223], v[88:91], v[208:211]
	v_mfma_f32_16x16x32_bf16 v[92:95], v[224:227], v[88:91], v[176:179]
	v_mfma_f32_16x16x32_bf16 v[84:87], v[228:231], v[88:91], v[184:187]
	v_mfma_f32_16x16x32_bf16 v[88:91], v[232:235], v[88:91], v[52:55]
	s_waitcnt lgkmcnt(1)
	v_mfma_f32_16x16x32_bf16 v[80:83], v[220:223], v[64:67], v[192:195]
	v_mfma_f32_16x16x32_bf16 v[76:79], v[224:227], v[64:67], v[180:183]
	v_mfma_f32_16x16x32_bf16 v[72:75], v[228:231], v[64:67], v[200:203]
	v_mfma_f32_16x16x32_bf16 v[68:71], v[232:235], v[64:67], v[188:191]
	s_waitcnt lgkmcnt(0)
	v_mfma_f32_16x16x32_bf16 v[64:67], v[220:223], v[152:155], v[56:59]
	v_mfma_f32_16x16x32_bf16 v[60:63], v[224:227], v[152:155], v[204:207]
	v_mfma_f32_16x16x32_bf16 v[56:59], v[228:231], v[152:155], v[212:215]
	v_mfma_f32_16x16x32_bf16 v[52:55], v[232:235], v[152:155], v[216:219]
	v_add_u32_e32 v149, s14, v157
	v_cmp_lt_i32_e32 vcc, v149, v156
	v_lshlrev_b32_e32 v154, 1, v140
	v_lshlrev_b32_e32 v152, 1, v142
	s_and_saveexec_b64 s[8:9], vcc
	s_cbranch_execz .LBB0_908
	v_add_u32_e32 v164, v141, v149
	v_ashrrev_i32_e32 v165, 31, v164
	v_readlane_b32 s10, v254, 3
	v_lshlrev_b64 v[164:165], 11, v[164:165]
	v_readlane_b32 s11, v254, 4
	v_mov_b32_e32 v155, v133
	v_mov_b32_e32 v153, v133
	v_lshl_add_u64 v[164:165], s[10:11], 0, v[164:165]
	v_lshl_add_u64 v[164:165], s[6:7], 1, v[164:165]
	v_lshl_add_u64 v[164:165], v[164:165], 0, v[154:155]
	v_lshl_add_u64 v[164:165], v[164:165], 0, v[152:153]
	v_cvt_pk_bf16_f32 v116, v116, v117
	v_cvt_pk_bf16_f32 v117, v118, v119
	v_cvt_pk_bf16_f32 v118, v128, v129
	v_cvt_pk_bf16_f32 v119, v130, v131
	global_store_dwordx4 v[164:165], v[116:119], off
	s_nop 1
	v_cvt_pk_bf16_f32 v116, v120, v121
	v_cvt_pk_bf16_f32 v117, v122, v123
	v_cvt_pk_bf16_f32 v118, v124, v125
	v_cvt_pk_bf16_f32 v119, v126, v127
	global_store_dwordx4 v[164:165], v[116:119], off offset:16

.LBB0_2357:
	s_add_i32 s47, s24, s3
	s_cmp_lt_i32 s47, s2
	s_cselect_b64 s[20:21], -1, 0
	s_cmp_ge_i32 s47, s2
	s_cselect_b64 s[8:9], -1, 0
	s_and_b64 vcc, exec, s[8:9]
	s_mov_b32 s10, s6
	s_mov_b32 s48, s7
	s_mov_b32 s49, s25
	v_mov_b32_e32 v176, v166
	s_waitcnt lgkmcnt(5)
	v_mov_b32_e32 v175, v139
	s_getreg_b32 s12, hwreg(HW_REG_HW_ID, 0, 6)
	s_lshl_b32 s12, s12, 2
	s_add_i32 s12, s12, 0x27000
	v_mov_b32_e32 v177, s12
	ds_read_b32 v177, v177
	s_cbranch_vccnz .LBB0_2361
	v_mbcnt_lo_u32_b32 v52, -1, 0
	v_mbcnt_hi_u32_b32 v52, -1, v52
	v_lshlrev_b32_e32 v52, 4, v52
	v_add_u32_e32 v52, 0x1f024, v52
	ds_read_b32 v53, v52
	ds_read_b32 v54, v52 offset:4
	ds_read_b32 v55, v52 offset:8
	ds_read_b32 v52, v52 offset:12
	s_ashr_i32 s11, s47, 2
	s_waitcnt lgkmcnt(0)
	v_cmp_ge_i32_e64 s[12:13], s11, v53
	v_cmp_ge_i32_e64 s[14:15], s11, v54
	s_bcnt1_i32_b64 s10, s[12:13]
	s_bcnt1_i32_b64 s12, s[14:15]
	s_add_i32 s10, s10, s12
	v_cmp_ge_i32_e64 s[12:13], s11, v55
	v_cmp_ge_i32_e64 s[14:15], s11, v52
	s_bcnt1_i32_b64 s12, s[12:13]
	s_bcnt1_i32_b64 s14, s[14:15]
	s_add_i32 s10, s10, s12
	s_add_i32 s10, s10, s14
	s_lshl_b32 s11, s10, 2
	s_add_i32 s11, s11, 0x1e800
	v_mov_b32_e32 v52, s11
	ds_read_b32 v53, v52
	ds_read_b32 v175, v52 offset:1040
	ds_read_b32 v176, v52 offset:2080
	ds_read_b32 v52, v52 offset:2084
	s_waitcnt lgkmcnt(0)
	v_readfirstlane_b32 s11, v176
	v_readfirstlane_b32 s12, v52
	v_readfirstlane_b32 s13, v53
	s_sub_i32 s12, s12, s11
	s_cmp_gt_u32 s12, 2
	s_cbranch_scc1 .Lopt24_m11_orig
	s_lshl_b32 s11, s11, 2
	s_sub_i32 s11, s47, s11
	s_and_b32 s48, s11, 3
	s_lshr_b32 s11, s11, 2
	s_add_i32 s13, s13, s12
	s_add_i32 s13, s13, -1
	s_add_i32 s12, s12, -1
	s_lshr_b32 s13, s13, s12
	s_mul_i32 s49, s11, s13
	s_add_i32 s13, s49, s13
	v_min_i32_e32 v176, s13, v53
	s_branch .LBB0_2361
.Lopt24_m11_orig:
	s_lshl_b32 s11, s10, 2
	s_add_i32 s11, s11, 0
	s_add_i32 s12, s11, 0x1f020
	v_mov_b32_e32 v52, s12
	ds_read2_b32 v[52:53], v52 offset1:1
	s_add_i32 s12, s11, 0x1e800
	s_add_i32 s11, s11, 0x1ec10
	v_mov_b32_e32 v54, s12
	v_mov_b32_e32 v55, s11
	s_waitcnt lgkmcnt(0)
	v_readfirstlane_b32 s11, v52
	v_readfirstlane_b32 s12, v53
	s_sub_i32 s12, s12, s11
	s_abs_i32 s15, s12
	v_cvt_f32_u32_e32 v52, s15
	s_lshl_b32 s11, s11, 2
	s_sub_i32 s11, s47, s11
	ds_read_b32 v54, v54
	ds_read_b32 v175, v55
	v_rcp_iflag_f32_e32 v52, v52
	s_ashr_i32 s13, s11, 31
	s_lshr_b32 s13, s13, 30
	s_add_i32 s13, s11, s13
	v_mul_f32_e32 v52, 0x4f7ffffe, v52
	v_cvt_u32_f32_e32 v52, v52
	s_ashr_i32 s14, s13, 2
	s_and_b32 s13, s13, -4
	s_sub_i32 s48, s11, s13
	s_waitcnt lgkmcnt(1)
	v_readfirstlane_b32 s11, v54
	s_sub_i32 s13, 0, s15
	v_readfirstlane_b32 s16, v52
	s_add_i32 s11, s11, s12
	s_mul_i32 s13, s13, s16
	s_add_i32 s11, s11, -1
	s_mul_hi_u32 s13, s16, s13
	s_xor_b32 s12, s11, s12
	s_abs_i32 s11, s11
	s_add_i32 s16, s16, s13
	s_mul_hi_u32 s13, s11, s16
	s_mul_i32 s16, s13, s15
	s_sub_i32 s11, s11, s16
	s_ashr_i32 s12, s12, 31
	s_add_i32 s16, s13, 1
	s_sub_i32 s17, s11, s15
	s_cmp_ge_u32 s11, s15
	s_cselect_b32 s13, s16, s13
	s_cselect_b32 s11, s17, s11
	s_add_i32 s16, s13, 1
	s_cmp_ge_u32 s11, s15
	s_cselect_b32 s11, s16, s13
	s_xor_b32 s11, s11, s12
	s_sub_i32 s11, s11, s12
	s_mul_i32 s49, s14, s11
	s_add_i32 s11, s49, s11
	v_min_i32_e32 v176, s11, v54
.LBB0_2361:
	s_waitcnt lgkmcnt(0)
	v_mov_b32_e32 v52, v177
	v_cndmask_b32_e64 v177, 0, 1, s[20:21]
	v_mov_b32_e32 v53, v133
	v_readfirstlane_b32 s11, v177
	s_xor_b32 s50, s26, s11
	s_waitcnt lgkmcnt(0)
	v_readfirstlane_b32 s11, v52
	v_mbcnt_lo_u32_b32 v52, -1, v53
	v_mbcnt_hi_u32_b32 v52, -1, v52
	v_lshl_or_b32 v52, s11, 6, v52
	s_waitcnt vmcnt(7)
	v_cvt_pk_bf16_f32 v20, v20, v21
	v_lshrrev_b32_e32 v55, 3, v52
	v_lshlrev_b32_e32 v56, 4, v52
	v_and_b32_e32 v56, 0x70, v56
	v_mul_lo_u32 v55, v55, s38
	v_ashrrev_i32_e32 v54, 5, v52
	v_add3_u32 v57, 0, v56, v55
	ds_write_b128 v57, v[36:39]
	ds_write_b128 v57, v[32:35] offset:9216
	s_waitcnt vmcnt(6)
	ds_write_b128 v57, v[44:47] offset:18432
	s_waitcnt vmcnt(5)
	ds_write_b128 v57, v[40:43] offset:27648
	s_waitcnt vmcnt(4)
	ds_write_b128 v57, v[48:51] offset:36864
	v_lshrrev_b32_e32 v34, 1, v54
	v_bfe_u32 v32, v52, 2, 3
	v_and_b32_e32 v33, 3, v54
	v_and_b32_e32 v34, 4, v34
	v_bitop3_b32 v32, v34, v32, v33 bitop3:0x36
	v_lshlrev_b32_e32 v33, 2, v52
	v_and_b32_e32 v57, 12, v33
	v_lshlrev_b32_e32 v58, 1, v57
	v_lshl_or_b32 v59, v32, 5, v58
	v_lshlrev_b32_e32 v54, 8, v54
	v_cvt_pk_bf16_f32 v21, v22, v23
	v_add3_u32 v22, s39, v59, v54
	s_waitcnt vmcnt(6)
	v_cvt_pk_bf16_f32 v16, v16, v17
	v_cvt_pk_bf16_f32 v17, v18, v19
	ds_write2st64_b64 v22, v[20:21], v[16:17] offset1:8
	s_waitcnt vmcnt(5)
	v_cvt_pk_bf16_f32 v16, v28, v29
	v_cvt_pk_bf16_f32 v17, v30, v31
	s_waitcnt vmcnt(4)
	v_cvt_pk_bf16_f32 v18, v24, v25
	v_cvt_pk_bf16_f32 v19, v26, v27
	s_mul_i32 s11, s26, 0x2800
	ds_write2st64_b64 v22, v[16:17], v[18:19] offset0:16 offset1:24
	v_add_u32_e32 v16, s11, v174
	v_add_u32_e32 v217, s11, v168
	v_add_u32_e32 v218, 48, v16
	ds_read_b32 v132, v217
	ds_read2st64_b32 v[16:17], v218 offset0:20 offset1:28
	ds_read2st64_b32 v[22:23], v218 offset0:36 offset1:44
	v_bfe_u32 v25, v52, 2, 2
	v_bfe_u32 v26, v52, 6, 1
	s_waitcnt lgkmcnt(2)
	v_lshl_add_u64 v[18:19], v[132:133], 1, s[92:93]
	s_waitcnt lgkmcnt(1)
	v_mov_b32_e32 v132, v16
	v_lshl_add_u64 v[20:21], v[132:133], 1, s[92:93]
	v_mov_b32_e32 v132, v17
	v_lshl_add_u64 v[16:17], v[132:133], 1, s[92:93]
	s_waitcnt lgkmcnt(0)
	v_mov_b32_e32 v132, v22
	global_load_dwordx4 v[44:47], v[18:19], off offset:128
	global_load_dwordx4 v[36:39], v[20:21], off offset:128
	v_lshl_add_u64 v[18:19], v[132:133], 1, s[92:93]
	v_mov_b32_e32 v132, v23
	global_load_dwordx4 v[40:43], v[16:17], off offset:128
	global_load_dwordx4 v[32:35], v[18:19], off offset:128
	v_lshl_add_u64 v[16:17], v[132:133], 1, s[92:93]
	global_load_dwordx4 v[48:51], v[16:17], off offset:128
	v_lshrrev_b32_e32 v18, 2, v52
	v_and_b32_e32 v18, 4, v18
	v_lshrrev_b32_e32 v16, 1, v52
	v_or_b32_e32 v19, v18, v25
	v_and_b32_e32 v16, 24, v16
	v_lshlrev_b32_e32 v20, 6, v26
	v_lshlrev_b32_e32 v19, 4, v19
	v_lshlrev_b32_e32 v23, 2, v26
	v_or_b32_e32 v17, v16, v25
	v_xor_b32_e32 v19, v19, v20
	v_or_b32_e32 v26, 1, v23
	v_or_b32_e32 v27, 2, v23
	v_or_b32_e32 v23, 3, v23
	v_or_b32_e32 v19, v19, v57
	v_lshlrev_b32_e32 v17, 8, v17
	v_bitop3_b32 v26, v18, v26, v25 bitop3:0x36
	v_bitop3_b32 v27, v18, v27, v25 bitop3:0x36
	v_bitop3_b32 v18, v18, v23, v25 bitop3:0x36
	v_ashrrev_i32_e32 v53, 7, v52
	v_add_u32_e32 v20, s39, v17
	v_lshlrev_b32_e32 v19, 1, v19
	v_lshl_or_b32 v26, v26, 5, v58
	v_lshl_or_b32 v27, v27, 5, v58
	v_lshl_or_b32 v18, v18, 5, v58
	s_lshl_b32 s12, s7, 6
	v_and_b32_e32 v24, 15, v52
	v_add_u32_e32 v213, v20, v19
	v_add_u32_e32 v214, v20, v26
	v_add_u32_e32 v211, v20, v27
	v_add_u32_e32 v145, v20, v18
	v_mul_lo_u32 v20, v53, s37
	s_ashr_i32 s13, s12, 31
	v_add_u32_e32 v21, 0, v17
	v_or_b32_e32 v20, v20, v24
	s_cmpk_lt_i32 s10, 0x100
	v_add_u32_e32 v22, 0x16c00, v21
	v_lshlrev_b32_e32 v16, 1, v16
	v_mul_lo_u32 v20, v20, s38
	s_cselect_b64 s[14:15], -1, 0
	s_cmpk_gt_i32 s10, 0xff
	v_readlane_b32 s76, v253, 4
	v_add_u32_e32 v216, v22, v19
	v_add_u32_e32 v215, v22, v26
	v_add_u32_e32 v212, v22, v27
	v_add_u32_e32 v147, v22, v18
	v_add3_u32 v178, 0, v16, v20
	v_add3_u32 v16, 0, v54, v59
	v_add_u32_e32 v22, 0x18c00, v21
	s_cselect_b64 s[16:17], -1, 0
	s_ashr_i32 s11, s10, 31
	v_readlane_b32 s84, v253, 12
	v_readlane_b32 s85, v253, 13
	v_add_u32_e32 v209, 0x1b800, v16
	v_add_u32_e32 v208, 0x1c800, v16
	v_add_u32_e32 v206, 0x1d800, v16
	v_or_b32_e32 v20, 0x2000, v17
	v_add_u32_e32 v207, v22, v19
	v_add_u32_e32 v204, v22, v26
	v_add_u32_e32 v201, v22, v27
	v_add_u32_e32 v199, v22, v18
	v_add_u32_e32 v22, 0x1ac00, v21
	v_add_u32_e32 v220, 0x17800, v16
	v_add_u32_e32 v221, 0x18800, v16
	v_add_u32_e32 v222, 0x19800, v16
	v_add_u32_e32 v16, 0x1cc00, v21
	s_lshl_b64 s[18:19], s[10:11], 16
	v_add_u32_e32 v21, s49, v141
	v_readlane_b32 s86, v253, 14
	v_readlane_b32 s87, v253, 15
	v_readlane_b32 s88, v253, 16
	v_readlane_b32 s89, v253, 17
	v_readlane_b32 s90, v253, 18
	v_readlane_b32 s91, v253, 19
	s_mov_b64 s[56:57], s[84:85]
	v_add3_u32 v205, s39, v19, v20
	v_add3_u32 v203, s39, v26, v20
	v_add3_u32 v200, s39, v27, v20
	v_add3_u32 v198, s39, v18, v20
	v_add_u32_e32 v17, s40, v17
	v_add_u32_e32 v194, v22, v19
	v_add_u32_e32 v191, v22, v26
	v_add_u32_e32 v189, v22, v27
	v_add_u32_e32 v188, v22, v18
	v_add3_u32 v185, s40, v19, v20
	v_add3_u32 v183, s40, v26, v20
	v_add3_u32 v181, s40, v27, v20
	v_add3_u32 v179, s40, v18, v20
	v_add_u32_e32 v20, -1, v176
	s_cmpk_lt_i32 s6, 0x100
	v_add_u32_e32 v22, 0x80, v21
	s_mov_b64 s[58:59], s[86:87]
	v_add_u32_e32 v187, v17, v18
	v_add_u32_e32 v186, v16, v19
	v_add_u32_e32 v184, v16, v26
	v_add_u32_e32 v182, v16, v27
	v_add_u32_e32 v180, v16, v18
	v_min_i32_e32 v16, v21, v20
	v_add_u32_e32 v18, 64, v21
	v_min_i32_e32 v148, v22, v20
	v_add_u32_e32 v22, 0xc0, v21
	v_add_u32_e32 v21, 0x100, v21
	s_cselect_b32 s22, s6, 1
	s_cselect_b32 s53, s27, s56
	s_cselect_b32 s54, s28, s57
	s_cselect_b32 s56, s33, s59
	v_min_i32_e32 v18, v18, v20
	v_min_i32_e32 v150, v22, v20
	v_min_i32_e32 v152, v21, v20
	s_cselect_b32 s55, s29, s58
	s_ashr_i32 s23, s22, 31
	v_mov_b32_e32 v20, s56
	v_mov_b32_e32 v21, s54
	s_lshl_b64 s[22:23], s[22:23], 20
	v_cndmask_b32_e64 v21, v20, v21, s[4:5]
	v_mov_b32_e32 v20, s55
	v_readlane_b32 s54, v253, 61
	v_readlane_b32 s55, v253, 62
	s_add_u32 s18, s54, s18
	v_add_u32_e32 v193, v17, v19
	v_add_u32_e32 v190, v17, v26
	v_add_u32_e32 v192, v17, v27
	v_ashrrev_i32_e32 v17, 31, v16
	v_ashrrev_i32_e32 v19, 31, v18
	v_ashrrev_i32_e32 v149, 31, v148
	v_ashrrev_i32_e32 v151, 31, v150
	v_ashrrev_i32_e32 v153, 31, v152
	s_addc_u32 s19, s55, s19
	v_mov_b32_e32 v22, s53
	v_lshl_add_u64 v[154:155], v[16:17], 2, s[18:19]
	v_lshl_add_u64 v[156:157], v[18:19], 2, s[18:19]
	v_lshl_add_u64 v[158:159], v[148:149], 2, s[18:19]
	v_lshl_add_u64 v[160:161], v[150:151], 2, s[18:19]
	v_lshl_add_u64 v[162:163], v[152:153], 2, s[18:19]
	s_and_b64 s[98:99], s[20:21], s[14:15]
	s_cbranch_scc0 .Lopt1_m11_skip
	global_load_dword v224, v[154:155], off
	global_load_dword v225, v[156:157], off
	global_load_dword v226, v[158:159], off
	global_load_dword v227, v[160:161], off
	global_load_dword v228, v[162:163], off

.LBB0_2481:
	s_add_i32 s25, s12, s1
	s_cmp_lt_i32 s25, s0
	s_cselect_b64 s[4:5], -1, 0
	s_cmp_ge_i32 s25, s0
	s_cselect_b64 s[2:3], -1, 0
	s_and_b64 vcc, exec, s[2:3]
	s_mov_b32 s26, s13
	s_mov_b32 s27, s15
	s_mov_b32 s28, s14
	v_mov_b32_e32 v163, v156
	v_mov_b32_e32 v162, v141
	s_getreg_b32 s6, hwreg(HW_REG_HW_ID, 0, 6)
	s_lshl_b32 s6, s6, 2
	s_add_i32 s6, s6, 0x27000
	v_mov_b32_e32 v244, s6
	ds_read_b32 v244, v244
	s_cbranch_vccnz .LBB0_2485
	v_mbcnt_lo_u32_b32 v52, -1, 0
	v_mbcnt_hi_u32_b32 v52, -1, v52
	v_lshlrev_b32_e32 v52, 4, v52
	v_add_u32_e32 v52, 0x1f024, v52
	ds_read_b32 v53, v52
	ds_read_b32 v54, v52 offset:4
	ds_read_b32 v55, v52 offset:8
	ds_read_b32 v52, v52 offset:12
	s_ashr_i32 s6, s25, 3
	s_waitcnt lgkmcnt(0)
	v_cmp_ge_i32_e64 s[8:9], s6, v53
	v_cmp_ge_i32_e64 s[10:11], s6, v54
	s_bcnt1_i32_b64 s26, s[8:9]
	s_bcnt1_i32_b64 s8, s[10:11]
	s_add_i32 s26, s26, s8
	v_cmp_ge_i32_e64 s[8:9], s6, v55
	v_cmp_ge_i32_e64 s[10:11], s6, v52
	s_bcnt1_i32_b64 s8, s[8:9]
	s_bcnt1_i32_b64 s10, s[10:11]
	s_add_i32 s26, s26, s8
	s_add_i32 s26, s26, s10
	s_lshl_b32 s6, s26, 2
	s_add_i32 s6, s6, 0x1e800
	v_mov_b32_e32 v52, s6
	ds_read_b32 v53, v52
	ds_read_b32 v162, v52 offset:1040
	ds_read_b32 v163, v52 offset:2080
	ds_read_b32 v52, v52 offset:2084
	s_waitcnt lgkmcnt(0)
	v_readfirstlane_b32 s6, v163
	v_readfirstlane_b32 s7, v52
	v_readfirstlane_b32 s8, v53
	s_sub_i32 s7, s7, s6
	s_cmp_gt_u32 s7, 2
	s_cbranch_scc1 .Lopt24_m21_orig
	s_lshl_b32 s6, s6, 3
	s_sub_i32 s6, s25, s6
	s_and_b32 s27, s6, 7
	s_lshr_b32 s6, s6, 3
	s_add_i32 s8, s8, s7
	s_add_i32 s8, s8, -1
	s_add_i32 s7, s7, -1
	s_lshr_b32 s8, s8, s7
	s_mul_i32 s28, s6, s8
	s_add_i32 s8, s28, s8
	v_min_i32_e32 v163, s8, v53
	s_branch .LBB0_2485
.Lopt24_m21_orig:
	s_lshl_b32 s6, s26, 2
	s_add_i32 s6, s6, 0
	s_add_i32 s7, s6, 0x1f020
	v_mov_b32_e32 v52, s7
	ds_read2_b32 v[52:53], v52 offset1:1
	s_add_i32 s7, s6, 0x1e800
	s_add_i32 s6, s6, 0x1ec10
	v_mov_b32_e32 v54, s7
	v_mov_b32_e32 v55, s6
	s_waitcnt lgkmcnt(0)
	v_readfirstlane_b32 s6, v52
	v_readfirstlane_b32 s7, v53
	s_sub_i32 s7, s7, s6
	s_abs_i32 s10, s7
	v_cvt_f32_u32_e32 v52, s10
	s_lshl_b32 s6, s6, 3
	s_sub_i32 s6, s25, s6
	ds_read_b32 v54, v54
	ds_read_b32 v162, v55
	v_rcp_iflag_f32_e32 v52, v52
	s_ashr_i32 s8, s6, 31
	s_lshr_b32 s8, s8, 29
	s_add_i32 s8, s6, s8
	v_mul_f32_e32 v52, 0x4f7ffffe, v52
	v_cvt_u32_f32_e32 v52, v52
	s_ashr_i32 s9, s8, 3
	s_and_b32 s8, s8, -8
	s_sub_i32 s27, s6, s8
	s_waitcnt lgkmcnt(1)
	v_readfirstlane_b32 s6, v54
	s_sub_i32 s8, 0, s10
	v_readfirstlane_b32 s11, v52
	s_add_i32 s6, s6, s7
	s_mul_i32 s8, s8, s11
	s_add_i32 s6, s6, -1
	s_mul_hi_u32 s8, s11, s8
	s_xor_b32 s7, s6, s7
	s_abs_i32 s6, s6
	s_add_i32 s11, s11, s8
	s_mul_hi_u32 s8, s6, s11
	s_mul_i32 s11, s8, s10
	s_sub_i32 s6, s6, s11
	s_ashr_i32 s7, s7, 31
	s_add_i32 s11, s8, 1
	s_sub_i32 s28, s6, s10
	s_cmp_ge_u32 s6, s10
	s_cselect_b32 s8, s11, s8
	s_cselect_b32 s6, s28, s6
	s_add_i32 s11, s8, 1
	s_cmp_ge_u32 s6, s10
	s_cselect_b32 s6, s11, s8
	s_xor_b32 s6, s6, s7
	s_sub_i32 s6, s6, s7
	s_mul_i32 s28, s9, s6
	s_add_i32 s6, s28, s6
	v_min_i32_e32 v163, s6, v54
.LBB0_2485:
	s_waitcnt lgkmcnt(0)
	v_mov_b32_e32 v52, v244
	v_mov_b32_e32 v53, 0
	s_waitcnt vmcnt(7)
	v_cvt_pk_bf16_f32 v20, v20, v21
	v_mbcnt_lo_u32_b32 v53, -1, v53
	v_mbcnt_hi_u32_b32 v53, -1, v53
	s_waitcnt lgkmcnt(0)
	v_readfirstlane_b32 s6, v52
	v_cvt_pk_bf16_f32 v21, v22, v23
	s_waitcnt vmcnt(6)
	v_cvt_pk_bf16_f32 v16, v16, v17
	v_lshl_or_b32 v62, s6, 6, v53
	v_cvt_pk_bf16_f32 v17, v18, v19
	v_lshrrev_b32_e32 v53, 3, v62
	v_lshlrev_b32_e32 v54, 4, v62
	v_and_b32_e32 v68, 0x70, v54
	v_mul_lo_u32 v69, v53, s22
	v_ashrrev_i32_e32 v52, 5, v62
	v_add3_u32 v53, 0, v68, v69
	ds_write_b128 v53, v[36:39]
	ds_write_b128 v53, v[32:35] offset:9216
	ds_write_b128 v53, v[44:47] offset:18432
	s_waitcnt vmcnt(5)
	ds_write_b128 v53, v[40:43] offset:27648
	s_waitcnt vmcnt(4)
	ds_write_b128 v53, v[48:51] offset:36864
	v_lshrrev_b32_e32 v34, 1, v52
	v_bfe_u32 v32, v62, 2, 3
	v_and_b32_e32 v33, 3, v52
	v_and_b32_e32 v34, 4, v34
	v_bitop3_b32 v32, v34, v32, v33 bitop3:0x36
	v_lshlrev_b32_e32 v33, 2, v62
	v_and_b32_e32 v36, 12, v33
	v_lshlrev_b32_e32 v37, 1, v36
	v_lshl_or_b32 v70, v32, 5, v37
	v_lshlrev_b32_e32 v172, 8, v52
	v_add3_u32 v22, s23, v70, v172
	ds_write2st64_b64 v22, v[20:21], v[16:17] offset1:8
	s_waitcnt vmcnt(5)
	v_cvt_pk_bf16_f32 v16, v28, v29
	v_cvt_pk_bf16_f32 v17, v30, v31
	s_waitcnt vmcnt(4)
	v_cvt_pk_bf16_f32 v18, v24, v25
	v_cvt_pk_bf16_f32 v19, v26, v27
	ds_write2st64_b64 v22, v[16:17], v[18:19] offset0:16 offset1:24
	v_sub_u32_e32 v16, v156, v143
	v_xad_u32 v32, s14, -1, v16
	v_add_u32_e32 v17, s14, v141
	v_lshrrev_b32_e32 v39, 2, v62
	v_bfe_u32 v65, v62, 2, 2
	v_min_i32_e32 v16, 0, v32
	v_add_u32_e32 v33, v17, v143
	v_and_b32_e32 v39, 4, v39
	v_bfe_u32 v66, v62, 6, 1
	v_add_u32_e32 v16, v16, v33
	v_or_b32_e32 v40, v39, v65
	v_ashrrev_i32_e32 v17, 31, v16
	v_lshlrev_b32_e32 v41, 6, v66
	v_lshlrev_b32_e32 v40, 4, v40
	v_lshlrev_b64 v[16:17], 9, v[16:17]
	v_lshrrev_b32_e32 v38, 1, v62
	v_xor_b32_e32 v40, v40, v41
	s_cmpk_lt_i32 s13, 0x100
	v_readlane_b32 s36, v253, 4
	v_lshl_add_u64 v[52:53], v[134:135], 0, v[16:17]
	v_min_i32_e32 v16, 64, v32
	v_and_b32_e32 v67, 24, v38
	v_or_b32_e32 v36, v40, v36
	s_cselect_b32 s6, s13, 1
	v_readlane_b32 s48, v253, 16
	v_readlane_b32 s49, v253, 17
	v_add_u32_e32 v16, v16, v33
	v_or_b32_e32 v38, v67, v65
	v_lshlrev_b32_e32 v188, 1, v36
	v_lshlrev_b32_e32 v36, 2, v66
	s_cselect_b32 s9, s17, s49
	s_cselect_b32 s8, s16, s48
	s_ashr_i32 s7, s6, 31
	v_ashrrev_i32_e32 v17, 31, v16
	v_lshlrev_b32_e32 v71, 8, v38
	v_or_b32_e32 v38, 1, v36
	s_lshl_b64 s[6:7], s[6:7], 20
	v_lshlrev_b64 v[16:17], 9, v[16:17]
	v_bitop3_b32 v38, v39, v38, v65 bitop3:0x36
	s_add_u32 s8, s8, s6
	v_lshl_add_u64 v[54:55], v[134:135], 0, v[16:17]
	v_min_i32_e32 v16, 0x80, v32
	v_lshl_or_b32 v192, v38, 5, v37
	v_or_b32_e32 v38, 2, v36
	v_or_b32_e32 v36, 3, v36
	s_addc_u32 s9, s9, s7
	s_lshl_b32 s6, s15, 7
	v_add_u32_e32 v16, v16, v33
	v_bitop3_b32 v38, v39, v38, v65 bitop3:0x36
	v_bitop3_b32 v36, v39, v36, v65 bitop3:0x36
	s_ashr_i32 s7, s6, 31
	v_ashrrev_i32_e32 v17, 31, v16
	v_lshl_or_b32 v193, v38, 5, v37
	v_lshl_or_b32 v196, v36, 5, v37
	v_lshl_add_u64 v[36:37], s[8:9], 0, v[144:145]
	s_lshl_b64 s[10:11], s[6:7], 2
	v_lshlrev_b64 v[16:17], 9, v[16:17]
	v_lshl_add_u64 v[36:37], v[36:37], 0, s[10:11]
	v_lshl_add_u64 v[56:57], v[134:135], 0, v[16:17]
	v_min_i32_e32 v16, 0xc0, v32
	v_min_i32_e32 v32, 0x100, v32
	v_lshl_add_u64 v[36:37], v[36:37], 0, v[132:133]
	v_mov_b32_e32 v149, v133
	v_add_u32_e32 v32, v32, v33
	v_lshl_add_u64 v[36:37], v[36:37], 0, v[148:149]
	v_mov_b32_e32 v151, v133
	v_add_u32_e32 v16, v16, v33
	v_ashrrev_i32_e32 v33, 31, v32
	v_lshl_add_u64 v[36:37], v[36:37], 0, v[150:151]
	v_ashrrev_i32_e32 v17, 31, v16
	v_lshlrev_b64 v[32:33], 9, v[32:33]
	v_add_co_u32_e32 v38, vcc, s18, v36
	v_lshlrev_b64 v[16:17], 9, v[16:17]
	v_lshl_add_u64 v[60:61], v[134:135], 0, v[32:33]
	v_addc_co_u32_e32 v39, vcc, 0, v37, vcc
	global_load_dwordx4 v[24:27], v[52:53], off offset:128
	global_load_dwordx4 v[28:31], v[54:55], off offset:128
	v_lshl_add_u64 v[58:59], v[134:135], 0, v[16:17]
	global_load_dwordx4 v[16:19], v[56:57], off offset:128
	global_load_dwordx4 v[20:23], v[58:59], off offset:128
	global_load_dwordx4 v[32:35], v[60:61], off offset:128
	s_waitcnt lgkmcnt(0)
	s_barrier
	global_load_dwordx4 v[48:51], v[36:37], off
	global_load_dwordx4 v[44:47], v[38:39], off
	v_add_co_u32_e32 v38, vcc, s19, v36
	v_ashrrev_i32_e32 v63, 7, v62
	s_nop 0
	v_addc_co_u32_e32 v39, vcc, 0, v37, vcc
	v_add_co_u32_e32 v36, vcc, s20, v36
	v_and_b32_e32 v64, 15, v62
	s_nop 0
	v_addc_co_u32_e32 v37, vcc, 0, v37, vcc
	global_load_dwordx4 v[40:43], v[38:39], off
	s_nop 0
	global_load_dwordx4 v[36:39], v[36:37], off
	v_add_u32_e32 v62, s23, v71
	v_add_u32_e32 v84, v62, v188
	v_add_u32_e32 v86, v62, v192
	v_add_u32_e32 v82, v62, v193
	v_add_u32_e32 v236, v62, v196
	v_mul_lo_u32 v62, v63, s21
	v_add_u32_e32 v189, 0, v71
	v_or_b32_e32 v62, v62, v64
	v_add_u32_e32 v72, 0x16c00, v189
	v_lshlrev_b32_e32 v63, 1, v67
	v_mul_lo_u32 v62, v62, s22
	v_add_u32_e32 v85, v72, v188
	v_add_u32_e32 v87, v72, v192
	v_add_u32_e32 v83, v72, v193
	v_add_u32_e32 v237, v72, v196
	v_add3_u32 v62, 0, v63, v62
	ds_read_b64_tr_b16 v[100:101], v84
	ds_read_b64_tr_b16 v[102:103], v85
	ds_read_b64_tr_b16 v[104:105], v86
	ds_read_b64_tr_b16 v[106:107], v87
	ds_read_b128 v[64:67], v62
	ds_read_b64_tr_b16 v[108:109], v82
	ds_read_b64_tr_b16 v[110:111], v83
	ds_read_b128 v[112:115], v62 offset:2304
	ds_read_b64_tr_b16 v[120:121], v236
	ds_read_b64_tr_b16 v[122:123], v237
	v_add3_u32 v63, 0, v172, v70
	v_or_b32_e32 v197, 0x2000, v71
	v_add_u32_e32 v72, 0x18c00, v189
	s_waitcnt lgkmcnt(5)
	v_mfma_f32_16x16x32_bf16 v[116:119], v[100:103], v[64:67], 0
	v_add3_u32 v79, 0, v69, v68
	v_add_u32_e32 v68, s24, v71
	ds_read_b128 v[176:179], v62 offset:4608
	ds_read_b128 v[180:183], v62 offset:6912
	v_mfma_f32_16x16x32_bf16 v[124:127], v[104:107], v[64:67], 0
	v_add3_u32 v99, s24, v172, v70
	v_add_u32_e32 v98, 0x1b800, v63
	v_add_u32_e32 v95, 0x1c800, v63
	s_waitcnt lgkmcnt(5)
	v_mfma_f32_16x16x32_bf16 v[128:131], v[108:111], v[64:67], 0
	v_add_u32_e32 v92, 0x1d800, v63
	v_add3_u32 v91, s23, v188, v197
	v_add_u32_e32 v93, v72, v188
	s_waitcnt lgkmcnt(2)
	v_mfma_f32_16x16x32_bf16 v[152:155], v[120:123], v[64:67], 0
	v_add_u32_e32 v64, 0x1ac00, v189
	v_add_u32_e32 v66, 0x1cc00, v189
	v_add3_u32 v89, s23, v192, v197
	v_add_u32_e32 v90, v72, v192
	v_add3_u32 v88, s23, v193, v197
	v_add_u32_e32 v94, v72, v193
	v_add3_u32 v96, s23, v196, v197
	v_add_u32_e32 v97, v72, v196
	v_add_u32_e32 v77, v68, v188
	v_add_u32_e32 v78, v64, v188
	v_add_u32_e32 v74, v68, v192
	v_mfma_f32_16x16x32_bf16 v[164:167], v[100:103], v[112:115], 0
	v_add_u32_e32 v75, v64, v192
	v_add_u32_e32 v76, v68, v193
	v_add_u32_e32 v71, v64, v193
	v_mfma_f32_16x16x32_bf16 v[168:171], v[104:107], v[112:115], 0
	v_add_u32_e32 v72, v68, v196
	v_add_u32_e32 v73, v64, v196
	v_add3_u32 v238, s23, v172, v70
	v_mfma_f32_16x16x32_bf16 v[172:175], v[108:111], v[112:115], 0
	v_add_u32_e32 v239, 0x17800, v63
	v_add_u32_e32 v240, 0x18800, v63
	v_add_u32_e32 v241, 0x19800, v63
	v_mfma_f32_16x16x32_bf16 v[112:115], v[120:123], v[112:115], 0
	v_add3_u32 v68, s24, v188, v197
	v_add_u32_e32 v70, v66, v188
	v_add3_u32 v67, s24, v192, v197
	v_add_u32_e32 v69, v66, v192
	v_add3_u32 v63, s24, v193, v197
	v_add_u32_e32 v64, v66, v193
	v_add3_u32 v65, s24, v196, v197
	v_add_u32_e32 v66, v66, v196
	ds_read_b128 v[196:199], v62 offset:9216
	v_add_u32_e32 v80, 0x12000, v79
	v_add_u32_e32 v81, 0x14400, v79
	s_waitcnt vmcnt(12)
	v_cvt_pk_bf16_f32 v12, v12, v13
	v_cvt_pk_bf16_f32 v13, v14, v15
	s_waitcnt vmcnt(11)
	v_cvt_pk_bf16_f32 v8, v8, v9
	v_cvt_pk_bf16_f32 v9, v10, v11
	v_readlane_b32 s37, v253, 5
	v_readlane_b32 s38, v253, 6
	v_readlane_b32 s39, v253, 7
	v_readlane_b32 s40, v253, 8
	v_readlane_b32 s41, v253, 9
	v_readlane_b32 s42, v253, 10
	v_readlane_b32 s43, v253, 11
	v_readlane_b32 s44, v253, 12
	v_readlane_b32 s45, v253, 13
	v_readlane_b32 s46, v253, 14
	v_readlane_b32 s47, v253, 15
	v_readlane_b32 s50, v253, 18
	v_readlane_b32 s51, v253, 19
	s_waitcnt lgkmcnt(2)
	v_mfma_f32_16x16x32_bf16 v[184:187], v[100:103], v[176:179], 0
	ds_write_b64 v99, v[12:13]
	ds_write_b64 v98, v[8:9]
	v_mfma_f32_16x16x32_bf16 v[188:191], v[104:107], v[176:179], 0
	v_mfma_f32_16x16x32_bf16 v[192:195], v[108:111], v[176:179], 0
	v_mfma_f32_16x16x32_bf16 v[176:179], v[120:123], v[176:179], 0
	ds_read_b128 v[204:207], v62 offset:64
	ds_read_b128 v[208:211], v62 offset:2368
	s_waitcnt vmcnt(9)
	v_cvt_pk_bf16_f32 v0, v0, v1
	v_cvt_pk_bf16_f32 v1, v2, v3
	s_waitcnt lgkmcnt(5)
	v_mfma_f32_16x16x32_bf16 v[8:11], v[100:103], v[180:183], 0
	ds_read_b128 v[212:215], v62 offset:4672
	v_cvt_pk_bf16_f32 v216, v4, v5
	v_cvt_pk_bf16_f32 v217, v6, v7
	v_mfma_f32_16x16x32_bf16 v[12:15], v[104:107], v[180:183], 0
	ds_write_b64 v92, v[0:1]
	ds_write_b64 v95, v[216:217]
	s_waitcnt lgkmcnt(7)
	v_mfma_f32_16x16x32_bf16 v[100:103], v[100:103], v[196:199], 0
	v_mfma_f32_16x16x32_bf16 v[104:107], v[104:107], v[196:199], 0
	v_mfma_f32_16x16x32_bf16 v[4:7], v[108:111], v[196:199], 0
	v_mfma_f32_16x16x32_bf16 v[0:3], v[120:123], v[196:199], 0
	v_mfma_f32_16x16x32_bf16 v[200:203], v[108:111], v[180:183], 0
	v_mfma_f32_16x16x32_bf16 v[180:183], v[120:123], v[180:183], 0
	ds_read_b64_tr_b16 v[108:109], v91
	ds_read_b64_tr_b16 v[110:111], v93
	ds_read_b64_tr_b16 v[120:121], v89
	ds_read_b64_tr_b16 v[122:123], v90
	ds_read_b64_tr_b16 v[196:197], v88
	ds_read_b64_tr_b16 v[198:199], v94
	ds_read_b64_tr_b16 v[216:217], v96
	ds_read_b64_tr_b16 v[218:219], v97
	s_waitcnt lgkmcnt(6)
	v_mfma_f32_16x16x32_bf16 v[116:119], v[108:111], v[204:207], v[116:119]
	s_waitcnt lgkmcnt(4)
	v_mfma_f32_16x16x32_bf16 v[124:127], v[120:123], v[204:207], v[124:127]
	s_waitcnt lgkmcnt(2)
	v_mfma_f32_16x16x32_bf16 v[128:131], v[196:199], v[204:207], v[128:131]
	s_waitcnt lgkmcnt(0)
	v_mfma_f32_16x16x32_bf16 v[152:155], v[216:219], v[204:207], v[152:155]
	v_mfma_f32_16x16x32_bf16 v[164:167], v[108:111], v[208:211], v[164:167]
	v_mfma_f32_16x16x32_bf16 v[168:171], v[120:123], v[208:211], v[168:171]
	v_mfma_f32_16x16x32_bf16 v[172:175], v[196:199], v[208:211], v[172:175]
	v_mfma_f32_16x16x32_bf16 v[112:115], v[216:219], v[208:211], v[112:115]
	ds_read_b128 v[204:207], v62 offset:6976
	ds_read_b128 v[208:211], v62 offset:9280
	s_waitcnt vmcnt(8)
	ds_write_b128 v79, v[24:27] offset:46080
	s_waitcnt vmcnt(7)
	ds_write_b128 v79, v[28:31] offset:55296
	v_mfma_f32_16x16x32_bf16 v[24:27], v[216:219], v[212:215], v[176:179]
	v_mfma_f32_16x16x32_bf16 v[184:187], v[108:111], v[212:215], v[184:187]
	v_mfma_f32_16x16x32_bf16 v[188:191], v[120:123], v[212:215], v[188:191]
	v_mfma_f32_16x16x32_bf16 v[192:195], v[196:199], v[212:215], v[192:195]
	s_waitcnt lgkmcnt(3)
	v_mfma_f32_16x16x32_bf16 v[8:11], v[108:111], v[204:207], v[8:11]
	v_mfma_f32_16x16x32_bf16 v[28:31], v[120:123], v[204:207], v[12:15]
	v_mfma_f32_16x16x32_bf16 v[176:179], v[196:199], v[204:207], v[200:203]
	v_mfma_f32_16x16x32_bf16 v[180:183], v[216:219], v[204:207], v[180:183]
	s_waitcnt lgkmcnt(2)
	v_mfma_f32_16x16x32_bf16 v[100:103], v[108:111], v[208:211], v[100:103]
	v_mfma_f32_16x16x32_bf16 v[104:107], v[120:123], v[208:211], v[104:107]
	global_load_dwordx4 v[108:111], v[52:53], off offset:256
	global_load_dwordx4 v[120:123], v[54:55], off offset:256
	global_load_dwordx4 v[200:203], v[56:57], off offset:256
	global_load_dwordx4 v[204:207], v[58:59], off offset:256
	global_load_dwordx4 v[212:215], v[60:61], off offset:256
	s_waitcnt vmcnt(11)
	ds_write_b128 v79, v[16:19] offset:64512
	s_waitcnt vmcnt(10)
	ds_write_b128 v80, v[20:23]
	s_waitcnt vmcnt(9)
	ds_write_b128 v81, v[32:35]
	v_mfma_f32_16x16x32_bf16 v[4:7], v[196:199], v[208:211], v[4:7]
	v_mfma_f32_16x16x32_bf16 v[0:3], v[216:219], v[208:211], v[0:3]
	s_waitcnt lgkmcnt(0)
	s_barrier
	ds_read_b64_tr_b16 v[16:17], v77
	ds_read_b64_tr_b16 v[18:19], v78
	ds_read_b128 v[12:15], v62 offset:46080
	ds_read_b64_tr_b16 v[20:21], v74
	ds_read_b64_tr_b16 v[22:23], v75
	ds_read_b64_tr_b16 v[196:197], v76
	ds_read_b128 v[32:35], v62 offset:48384
	ds_read_b128 v[208:211], v62 offset:55296
	ds_read_b64_tr_b16 v[198:199], v71
	ds_read_b64_tr_b16 v[216:217], v72
	ds_read_b64_tr_b16 v[218:219], v73
	s_waitcnt lgkmcnt(8)
	v_mfma_f32_16x16x32_bf16 v[116:119], v[16:19], v[12:15], v[116:119]
	ds_read_b128 v[220:223], v62 offset:50688
	s_waitcnt vmcnt(8)
	v_cvt_pk_bf16_f32 v48, v48, v49
	v_cvt_pk_bf16_f32 v49, v50, v51
	s_waitcnt lgkmcnt(7)
	v_mfma_f32_16x16x32_bf16 v[124:127], v[20:23], v[12:15], v[124:127]
	s_waitcnt vmcnt(7)
	v_cvt_pk_bf16_f32 v44, v44, v45
	v_cvt_pk_bf16_f32 v45, v46, v47
	s_waitcnt lgkmcnt(3)
	v_mfma_f32_16x16x32_bf16 v[128:131], v[196:199], v[12:15], v[128:131]
	s_waitcnt lgkmcnt(1)
	v_mfma_f32_16x16x32_bf16 v[152:155], v[216:219], v[12:15], v[152:155]
	v_lshl_add_u64 v[12:13], s[8:9], 0, v[146:147]
	v_lshl_add_u64 v[12:13], v[12:13], 0, s[10:11]
	v_lshl_add_u64 v[12:13], v[12:13], 0, v[132:133]
	v_lshl_add_u64 v[12:13], v[12:13], 0, v[148:149]
	v_lshl_add_u64 v[12:13], v[12:13], 0, v[150:151]
	v_add_co_u32_e32 v14, vcc, s18, v12
	v_mfma_f32_16x16x32_bf16 v[164:167], v[16:19], v[32:35], v[164:167]
	s_nop 0
	v_addc_co_u32_e32 v15, vcc, 0, v13, vcc
	global_load_dwordx4 v[224:227], v[12:13], off
	global_load_dwordx4 v[228:231], v[14:15], off
	v_add_co_u32_e32 v14, vcc, s19, v12
	v_mfma_f32_16x16x32_bf16 v[168:171], v[20:23], v[32:35], v[168:171]
	s_nop 0
	v_addc_co_u32_e32 v15, vcc, 0, v13, vcc
	v_add_co_u32_e32 v12, vcc, s20, v12
	v_mfma_f32_16x16x32_bf16 v[172:175], v[196:199], v[32:35], v[172:175]
	s_nop 0
	v_addc_co_u32_e32 v13, vcc, 0, v13, vcc
	ds_read_b128 v[232:235], v62 offset:52992
	v_mfma_f32_16x16x32_bf16 v[112:115], v[216:219], v[32:35], v[112:115]
	global_load_dwordx4 v[32:35], v[14:15], off
	s_nop 0
	global_load_dwordx4 v[12:15], v[12:13], off
	ds_write_b64 v238, v[48:49]
	ds_write_b64 v239, v[44:45]
	s_waitcnt lgkmcnt(3)
	v_mfma_f32_16x16x32_bf16 v[24:27], v[216:219], v[220:223], v[24:27]
	v_mfma_f32_16x16x32_bf16 v[184:187], v[16:19], v[220:223], v[184:187]
	v_mfma_f32_16x16x32_bf16 v[188:191], v[20:23], v[220:223], v[188:191]
	v_mfma_f32_16x16x32_bf16 v[192:195], v[196:199], v[220:223], v[192:195]
	s_waitcnt lgkmcnt(2)
	v_mfma_f32_16x16x32_bf16 v[8:11], v[16:19], v[232:235], v[8:11]
	v_mfma_f32_16x16x32_bf16 v[28:31], v[20:23], v[232:235], v[28:31]
	v_mfma_f32_16x16x32_bf16 v[44:47], v[196:199], v[232:235], v[176:179]
	v_mfma_f32_16x16x32_bf16 v[16:19], v[16:19], v[208:211], v[100:103]
	s_nop 2
	ds_read_b128 v[100:103], v62 offset:46144
	ds_read_b128 v[176:179], v62 offset:48448
	v_mfma_f32_16x16x32_bf16 v[20:23], v[20:23], v[208:211], v[104:107]
	s_nop 2
	ds_read_b128 v[104:107], v62 offset:50752
	v_mfma_f32_16x16x32_bf16 v[48:51], v[216:219], v[232:235], v[180:183]
	s_waitcnt vmcnt(10)
	s_nop 1
	v_cvt_pk_bf16_f32 v180, v40, v41
	v_cvt_pk_bf16_f32 v181, v42, v43
	v_mfma_f32_16x16x32_bf16 v[40:43], v[196:199], v[208:211], v[4:7]
	ds_write_b64 v240, v[180:181]
	s_waitcnt vmcnt(9)
	s_nop 0
	v_cvt_pk_bf16_f32 v4, v36, v37
	v_cvt_pk_bf16_f32 v5, v38, v39
	v_mfma_f32_16x16x32_bf16 v[36:39], v[216:219], v[208:211], v[0:3]
	ds_write_b64 v241, v[4:5]
	s_nop 1
	ds_read_b64_tr_b16 v[0:1], v68
	ds_read_b64_tr_b16 v[2:3], v70
	ds_read_b64_tr_b16 v[4:5], v67
	ds_read_b64_tr_b16 v[6:7], v69
	ds_read_b64_tr_b16 v[180:181], v63
	ds_read_b64_tr_b16 v[182:183], v64
	ds_read_b64_tr_b16 v[196:197], v65
	ds_read_b64_tr_b16 v[198:199], v66
	s_waitcnt lgkmcnt(6)
	v_mfma_f32_16x16x32_bf16 v[116:119], v[0:3], v[100:103], v[116:119]
	s_waitcnt lgkmcnt(4)
	v_mfma_f32_16x16x32_bf16 v[124:127], v[4:7], v[100:103], v[124:127]
	s_waitcnt lgkmcnt(2)
	v_mfma_f32_16x16x32_bf16 v[128:131], v[180:183], v[100:103], v[128:131]
	s_waitcnt lgkmcnt(0)
	v_mfma_f32_16x16x32_bf16 v[100:103], v[196:199], v[100:103], v[152:155]
	v_mfma_f32_16x16x32_bf16 v[152:155], v[0:3], v[176:179], v[164:167]
	v_mfma_f32_16x16x32_bf16 v[164:167], v[4:7], v[176:179], v[168:171]
	v_mfma_f32_16x16x32_bf16 v[168:171], v[180:183], v[176:179], v[172:175]
	v_mfma_f32_16x16x32_bf16 v[112:115], v[196:199], v[176:179], v[112:115]
	v_mfma_f32_16x16x32_bf16 v[172:175], v[0:3], v[104:107], v[184:187]
	v_mfma_f32_16x16x32_bf16 v[176:179], v[4:7], v[104:107], v[188:191]
	v_mfma_f32_16x16x32_bf16 v[184:187], v[180:183], v[104:107], v[192:195]
	s_nop 1
	ds_read_b128 v[188:191], v62 offset:53056
	ds_read_b128 v[192:195], v62 offset:55360
	s_waitcnt vmcnt(8)
	ds_write_b128 v79, v[108:111]
	s_waitcnt vmcnt(7)
	ds_write_b128 v79, v[120:123] offset:9216
	v_mfma_f32_16x16x32_bf16 v[104:107], v[196:199], v[104:107], v[24:27]
	s_waitcnt lgkmcnt(3)
	v_mfma_f32_16x16x32_bf16 v[108:111], v[0:3], v[188:191], v[8:11]
	v_mfma_f32_16x16x32_bf16 v[120:123], v[4:7], v[188:191], v[28:31]
	v_mfma_f32_16x16x32_bf16 v[44:47], v[180:183], v[188:191], v[44:47]
	v_mfma_f32_16x16x32_bf16 v[48:51], v[196:199], v[188:191], v[48:51]
	s_waitcnt lgkmcnt(2)
	v_mfma_f32_16x16x32_bf16 v[188:191], v[0:3], v[192:195], v[16:19]
	v_mfma_f32_16x16x32_bf16 v[208:211], v[4:7], v[192:195], v[20:23]
	global_load_dwordx4 v[216:219], v[52:53], off offset:384
	s_nop 0
	global_load_dwordx4 v[52:55], v[54:55], off offset:384
	s_nop 0
	global_load_dwordx4 v[0:3], v[56:57], off offset:384
	global_load_dwordx4 v[4:7], v[58:59], off offset:384
	global_load_dwordx4 v[8:11], v[60:61], off offset:384
	s_waitcnt vmcnt(11)
	ds_write_b128 v79, v[200:203] offset:18432
	s_waitcnt vmcnt(10)
	ds_write_b128 v79, v[204:207] offset:27648
	s_waitcnt vmcnt(9)
	ds_write_b128 v79, v[212:215] offset:36864
	v_mfma_f32_16x16x32_bf16 v[40:43], v[180:183], v[192:195], v[40:43]
	v_mfma_f32_16x16x32_bf16 v[36:39], v[196:199], v[192:195], v[36:39]
	s_cmpk_lt_i32 s26, 0x100
	s_cselect_b32 s8, s26, 1
	s_waitcnt lgkmcnt(0)
	s_barrier
	ds_read_b64_tr_b16 v[56:57], v84
	ds_read_b64_tr_b16 v[58:59], v85
	ds_read_b64_tr_b16 v[84:85], v86
	ds_read_b64_tr_b16 v[86:87], v87
	ds_read_b128 v[16:19], v62
	ds_read_b64_tr_b16 v[180:181], v82
	ds_read_b64_tr_b16 v[182:183], v83
	ds_read_b128 v[20:23], v62 offset:2304
	ds_read_b64_tr_b16 v[192:193], v236
	ds_read_b64_tr_b16 v[194:195], v237
	s_cselect_b32 s10, s17, s49
	s_cselect_b32 s11, s16, s48
	s_ashr_i32 s9, s8, 31
	s_lshl_b64 s[8:9], s[8:9], 20
	s_add_u32 s8, s11, s8
	s_addc_u32 s9, s10, s9
	s_lshl_b32 s10, s27, 7
	s_ashr_i32 s11, s10, 31
	s_waitcnt lgkmcnt(5)
	v_mfma_f32_16x16x32_bf16 v[116:119], v[56:59], v[16:19], v[116:119]
	s_lshl_b64 s[10:11], s[10:11], 2
	ds_read_b128 v[196:199], v62 offset:4608
	s_waitcnt vmcnt(8)
	v_cvt_pk_bf16_f32 v60, v224, v225
	v_mfma_f32_16x16x32_bf16 v[124:127], v[84:87], v[16:19], v[124:127]
	v_cvt_pk_bf16_f32 v61, v226, v227
	s_waitcnt lgkmcnt(4)
	v_mfma_f32_16x16x32_bf16 v[128:131], v[180:183], v[16:19], v[128:131]
	s_waitcnt lgkmcnt(1)
	v_mfma_f32_16x16x32_bf16 v[100:103], v[192:195], v[16:19], v[100:103]
	v_lshl_add_u64 v[16:17], s[8:9], 0, v[136:137]
	v_lshl_add_u64 v[16:17], v[16:17], 0, s[10:11]
	v_lshl_add_u64 v[16:17], v[16:17], 0, v[132:133]
	v_lshl_add_u64 v[16:17], v[16:17], 0, v[148:149]
	v_lshl_add_u64 v[24:25], v[16:17], 0, v[150:151]
	v_add_co_u32_e32 v16, vcc, s18, v24
	v_mfma_f32_16x16x32_bf16 v[152:155], v[56:59], v[20:23], v[152:155]
	s_nop 0
	v_addc_co_u32_e32 v17, vcc, 0, v25, vcc
	v_add_co_u32_e32 v26, vcc, s19, v24
	v_mfma_f32_16x16x32_bf16 v[164:167], v[84:87], v[20:23], v[164:167]
	s_nop 0
	v_addc_co_u32_e32 v27, vcc, 0, v25, vcc
	v_mfma_f32_16x16x32_bf16 v[168:171], v[180:183], v[20:23], v[168:171]
	v_mfma_f32_16x16x32_bf16 v[112:115], v[192:195], v[20:23], v[112:115]
	global_load_dwordx4 v[20:23], v[24:25], off
	s_nop 0
	global_load_dwordx4 v[16:19], v[16:17], off
	v_add_co_u32_e32 v24, vcc, s20, v24
	ds_read_b128 v[200:203], v62 offset:6912
	s_nop 0
	v_addc_co_u32_e32 v25, vcc, 0, v25, vcc
	global_load_dwordx4 v[28:31], v[26:27], off
	s_nop 0
	global_load_dwordx4 v[24:27], v[24:25], off
	ds_read_b128 v[204:207], v62 offset:9216
	s_waitcnt lgkmcnt(2)
	v_mfma_f32_16x16x32_bf16 v[104:107], v[192:195], v[196:199], v[104:107]
	ds_write_b64 v99, v[60:61]
	s_waitcnt vmcnt(11)
	v_cvt_pk_bf16_f32 v60, v228, v229
	v_cvt_pk_bf16_f32 v61, v230, v231
	v_mfma_f32_16x16x32_bf16 v[172:175], v[56:59], v[196:199], v[172:175]
	ds_write_b64 v98, v[60:61]
	v_mfma_f32_16x16x32_bf16 v[176:179], v[84:87], v[196:199], v[176:179]
	v_mfma_f32_16x16x32_bf16 v[184:187], v[180:183], v[196:199], v[184:187]
	s_waitcnt lgkmcnt(3)
	v_mfma_f32_16x16x32_bf16 v[108:111], v[56:59], v[200:203], v[108:111]
	s_waitcnt vmcnt(9)
	v_cvt_pk_bf16_f32 v12, v12, v13
	v_cvt_pk_bf16_f32 v13, v14, v15
	v_cvt_pk_bf16_f32 v32, v32, v33
	s_waitcnt lgkmcnt(2)
	v_mfma_f32_16x16x32_bf16 v[56:59], v[56:59], v[204:207], v[188:191]
	s_nop 2
	ds_read_b128 v[188:191], v62 offset:64
	ds_read_b128 v[196:199], v62 offset:2368
	v_cvt_pk_bf16_f32 v33, v34, v35
	v_mfma_f32_16x16x32_bf16 v[120:123], v[84:87], v[200:203], v[120:123]
	v_mfma_f32_16x16x32_bf16 v[44:47], v[180:183], v[200:203], v[44:47]
	v_mfma_f32_16x16x32_bf16 v[48:51], v[192:195], v[200:203], v[48:51]
	ds_read_b128 v[200:203], v62 offset:4672
	ds_write_b64 v92, v[12:13]
	ds_write_b64 v95, v[32:33]
	v_mfma_f32_16x16x32_bf16 v[82:85], v[84:87], v[204:207], v[208:211]
	v_mfma_f32_16x16x32_bf16 v[40:43], v[180:183], v[204:207], v[40:43]
	v_mfma_f32_16x16x32_bf16 v[12:15], v[192:195], v[204:207], v[36:39]
	ds_read_b64_tr_b16 v[32:33], v91
	ds_read_b64_tr_b16 v[34:35], v93
	ds_read_b64_tr_b16 v[180:181], v89
	ds_read_b64_tr_b16 v[182:183], v90
	ds_read_b64_tr_b16 v[86:87], v88
	ds_read_b64_tr_b16 v[88:89], v94
	ds_read_b64_tr_b16 v[94:95], v96
	ds_read_b64_tr_b16 v[96:97], v97
	s_waitcnt lgkmcnt(6)
	v_mfma_f32_16x16x32_bf16 v[90:93], v[32:35], v[188:191], v[116:119]
	s_waitcnt lgkmcnt(4)
	v_mfma_f32_16x16x32_bf16 v[116:119], v[180:183], v[188:191], v[124:127]
	s_waitcnt lgkmcnt(2)
	v_mfma_f32_16x16x32_bf16 v[124:127], v[86:89], v[188:191], v[128:131]
	v_mfma_f32_16x16x32_bf16 v[128:131], v[32:35], v[196:199], v[152:155]
	v_mfma_f32_16x16x32_bf16 v[152:155], v[180:183], v[196:199], v[164:167]
	v_mfma_f32_16x16x32_bf16 v[164:167], v[86:89], v[196:199], v[168:171]
	v_mfma_f32_16x16x32_bf16 v[168:171], v[32:35], v[200:203], v[172:175]
	v_mfma_f32_16x16x32_bf16 v[172:175], v[180:183], v[200:203], v[176:179]
	v_mfma_f32_16x16x32_bf16 v[176:179], v[86:89], v[200:203], v[184:187]
	ds_read_b128 v[36:39], v62 offset:6976
	s_nop 1
	ds_read_b128 v[184:187], v62 offset:9280
	s_waitcnt vmcnt(8)
	ds_write_b128 v79, v[216:219] offset:46080
	s_waitcnt vmcnt(7)
	ds_write_b128 v79, v[52:55] offset:55296
	s_waitcnt lgkmcnt(4)
	v_mfma_f32_16x16x32_bf16 v[98:101], v[94:97], v[188:191], v[100:103]
	v_mfma_f32_16x16x32_bf16 v[112:115], v[94:97], v[196:199], v[112:115]
	v_mfma_f32_16x16x32_bf16 v[52:55], v[94:97], v[200:203], v[104:107]
	v_sub_u32_e32 v60, v163, v143
	v_xad_u32 v192, s28, -1, v60
	v_add_u32_e32 v61, s28, v162
	s_waitcnt lgkmcnt(3)
	v_mfma_f32_16x16x32_bf16 v[102:105], v[32:35], v[36:39], v[108:111]
	v_min_i32_e32 v60, 0, v192
	s_nop 1
	v_add_u32_e32 v110, v61, v143
	v_mfma_f32_16x16x32_bf16 v[106:109], v[180:183], v[36:39], v[120:123]
	v_add_u32_e32 v60, v60, v110
	v_ashrrev_i32_e32 v61, 31, v60
	v_lshlrev_b64 v[60:61], 9, v[60:61]
	v_mfma_f32_16x16x32_bf16 v[120:123], v[86:89], v[36:39], v[44:47]
	s_nop 2
	v_min_i32_e32 v46, 64, v192
	v_add_u32_e32 v46, v46, v110
	v_ashrrev_i32_e32 v47, 31, v46
	v_lshl_add_u64 v[44:45], v[134:135], 0, v[60:61]
	v_mfma_f32_16x16x32_bf16 v[188:191], v[94:97], v[36:39], v[48:51]
	v_lshlrev_b64 v[36:37], 9, v[46:47]
	v_lshl_add_u64 v[46:47], v[134:135], 0, v[36:37]
	s_waitcnt lgkmcnt(2)
	v_mfma_f32_16x16x32_bf16 v[56:59], v[32:35], v[184:187], v[56:59]
	global_load_dwordx4 v[36:39], v[44:45], off
	global_load_dwordx4 v[32:35], v[46:47], off
	v_min_i32_e32 v44, 0x80, v192
	v_min_i32_e32 v48, 0x100, v192
	v_mfma_f32_16x16x32_bf16 v[86:89], v[86:89], v[184:187], v[40:43]
	v_add_u32_e32 v44, v44, v110
	v_add_u32_e32 v48, v48, v110
	v_ashrrev_i32_e32 v45, 31, v44
	v_min_i32_e32 v42, 0xc0, v192
	v_add_u32_e32 v42, v42, v110
	v_ashrrev_i32_e32 v43, 31, v42
	v_ashrrev_i32_e32 v49, 31, v48
	v_lshlrev_b64 v[44:45], 9, v[44:45]
	v_lshlrev_b64 v[42:43], 9, v[42:43]
	v_lshlrev_b64 v[48:49], 9, v[48:49]
	v_lshl_add_u64 v[40:41], v[134:135], 0, v[44:45]
	v_lshl_add_u64 v[42:43], v[134:135], 0, v[42:43]
	v_lshl_add_u64 v[48:49], v[134:135], 0, v[48:49]
	global_load_dwordx4 v[44:47], v[40:41], off
	s_nop 0
	global_load_dwordx4 v[40:43], v[42:43], off
	v_mfma_f32_16x16x32_bf16 v[82:85], v[180:183], v[184:187], v[82:85]
	global_load_dwordx4 v[48:51], v[48:49], off
	s_waitcnt vmcnt(11)
	ds_write_b128 v79, v[0:3] offset:64512
	s_waitcnt vmcnt(10)
	ds_write_b128 v80, v[4:7]
	s_waitcnt vmcnt(9)
	ds_write_b128 v81, v[8:11]
	v_mfma_f32_16x16x32_bf16 v[94:97], v[94:97], v[184:187], v[12:15]
	s_waitcnt lgkmcnt(0)
	s_barrier
	ds_read_b64_tr_b16 v[180:181], v77
	ds_read_b64_tr_b16 v[182:183], v78
	ds_read_b128 v[0:3], v62 offset:46080
	ds_read_b64_tr_b16 v[78:79], v74
	ds_read_b64_tr_b16 v[80:81], v75
	ds_read_b64_tr_b16 v[74:75], v76
	ds_read_b128 v[4:7], v62 offset:48384
	ds_read_b128 v[184:187], v62 offset:55296
	ds_read_b64_tr_b16 v[76:77], v71
	ds_read_b64_tr_b16 v[192:193], v72
	ds_read_b64_tr_b16 v[194:195], v73
	s_waitcnt lgkmcnt(8)
	v_mfma_f32_16x16x32_bf16 v[90:93], v[180:183], v[0:3], v[90:93]
	s_waitcnt lgkmcnt(6)
	v_mfma_f32_16x16x32_bf16 v[116:119], v[78:81], v[0:3], v[116:119]
	s_waitcnt lgkmcnt(2)
	v_mfma_f32_16x16x32_bf16 v[196:199], v[74:77], v[0:3], v[124:127]
	s_waitcnt lgkmcnt(0)
	v_mfma_f32_16x16x32_bf16 v[98:101], v[192:195], v[0:3], v[98:101]
	v_lshl_add_u64 v[0:1], s[8:9], 0, v[138:139]
	v_lshl_add_u64 v[0:1], v[0:1], 0, s[10:11]
	v_lshl_add_u64 v[0:1], v[0:1], 0, v[132:133]
	v_lshl_add_u64 v[0:1], v[0:1], 0, v[148:149]
	v_lshl_add_u64 v[0:1], v[0:1], 0, v[150:151]
	v_add_co_u32_e32 v2, vcc, s18, v0
	ds_read_b128 v[124:127], v62 offset:50688
	s_nop 0
	v_addc_co_u32_e32 v3, vcc, 0, v1, vcc
	global_load_dwordx4 v[12:15], v[0:1], off
	global_load_dwordx4 v[8:11], v[2:3], off
	v_add_co_u32_e32 v2, vcc, s19, v0
	v_mfma_f32_16x16x32_bf16 v[200:203], v[180:183], v[4:7], v[128:131]
	s_nop 0
	v_addc_co_u32_e32 v3, vcc, 0, v1, vcc
	v_add_co_u32_e32 v0, vcc, s20, v0
	v_mfma_f32_16x16x32_bf16 v[152:155], v[78:81], v[4:7], v[152:155]
	s_nop 0
	v_addc_co_u32_e32 v1, vcc, 0, v1, vcc
	v_mfma_f32_16x16x32_bf16 v[164:167], v[74:77], v[4:7], v[164:167]
	v_mfma_f32_16x16x32_bf16 v[204:207], v[192:195], v[4:7], v[112:115]
	s_nop 2
	ds_read_b128 v[110:113], v62 offset:52992
	global_load_dwordx4 v[4:7], v[2:3], off
	s_nop 0
	global_load_dwordx4 v[0:3], v[0:1], off
	s_waitcnt lgkmcnt(1)
	v_mfma_f32_16x16x32_bf16 v[52:55], v[192:195], v[124:127], v[52:55]
	v_mfma_f32_16x16x32_bf16 v[168:171], v[180:183], v[124:127], v[168:171]
	v_mfma_f32_16x16x32_bf16 v[172:175], v[78:81], v[124:127], v[172:175]
	v_mfma_f32_16x16x32_bf16 v[176:179], v[74:77], v[124:127], v[176:179]
	s_waitcnt lgkmcnt(0)
	v_mfma_f32_16x16x32_bf16 v[208:211], v[180:183], v[110:113], v[102:105]
	v_mfma_f32_16x16x32_bf16 v[212:215], v[78:81], v[110:113], v[106:109]
	v_mfma_f32_16x16x32_bf16 v[216:219], v[74:77], v[110:113], v[120:123]
	v_mfma_f32_16x16x32_bf16 v[56:59], v[180:183], v[184:187], v[56:59]
	v_mfma_f32_16x16x32_bf16 v[180:183], v[78:81], v[184:187], v[82:85]
	v_mfma_f32_16x16x32_bf16 v[220:223], v[74:77], v[184:187], v[86:89]
	ds_read_b128 v[72:75], v62 offset:46144
	ds_read_b128 v[76:79], v62 offset:48448
	ds_read_b128 v[80:83], v62 offset:50752
	v_mfma_f32_16x16x32_bf16 v[188:191], v[192:195], v[110:113], v[188:191]
	v_mfma_f32_16x16x32_bf16 v[184:187], v[192:195], v[184:187], v[94:97]
	ds_read_b64_tr_b16 v[192:193], v68
	ds_read_b64_tr_b16 v[194:195], v70
	ds_read_b64_tr_b16 v[224:225], v67
	ds_read_b64_tr_b16 v[226:227], v69
	ds_read_b64_tr_b16 v[228:229], v63
	ds_read_b64_tr_b16 v[230:231], v64
	ds_read_b64_tr_b16 v[232:233], v65
	ds_read_b64_tr_b16 v[234:235], v66
	s_waitcnt lgkmcnt(6)
	v_mfma_f32_16x16x32_bf16 v[124:127], v[192:195], v[72:75], v[90:93]
	s_waitcnt lgkmcnt(4)
	v_mfma_f32_16x16x32_bf16 v[108:111], v[224:227], v[76:79], v[152:155]
	ds_read_b128 v[64:67], v62 offset:53056
	s_nop 1
	ds_read_b128 v[152:155], v62 offset:55360
	v_mfma_f32_16x16x32_bf16 v[128:131], v[224:227], v[72:75], v[116:119]
	s_waitcnt lgkmcnt(4)
	v_mfma_f32_16x16x32_bf16 v[120:123], v[228:231], v[72:75], v[196:199]
	s_waitcnt lgkmcnt(2)
	v_mfma_f32_16x16x32_bf16 v[116:119], v[232:235], v[72:75], v[98:101]
	v_mfma_f32_16x16x32_bf16 v[112:115], v[192:195], v[76:79], v[200:203]
	v_mfma_f32_16x16x32_bf16 v[104:107], v[228:231], v[76:79], v[164:167]
	v_mfma_f32_16x16x32_bf16 v[100:103], v[232:235], v[76:79], v[204:207]
	v_mfma_f32_16x16x32_bf16 v[96:99], v[192:195], v[80:83], v[168:171]
	v_mfma_f32_16x16x32_bf16 v[92:95], v[224:227], v[80:83], v[172:175]
	v_mfma_f32_16x16x32_bf16 v[84:87], v[228:231], v[80:83], v[176:179]
	v_mfma_f32_16x16x32_bf16 v[88:91], v[232:235], v[80:83], v[52:55]
	s_waitcnt lgkmcnt(1)
	v_mfma_f32_16x16x32_bf16 v[80:83], v[192:195], v[64:67], v[208:211]
	v_mfma_f32_16x16x32_bf16 v[76:79], v[224:227], v[64:67], v[212:215]
	v_mfma_f32_16x16x32_bf16 v[72:75], v[228:231], v[64:67], v[216:219]
	v_mfma_f32_16x16x32_bf16 v[68:71], v[232:235], v[64:67], v[188:191]
	s_waitcnt lgkmcnt(0)
	v_mfma_f32_16x16x32_bf16 v[64:67], v[192:195], v[152:155], v[56:59]
	v_mfma_f32_16x16x32_bf16 v[60:63], v[224:227], v[152:155], v[180:183]
	v_mfma_f32_16x16x32_bf16 v[56:59], v[228:231], v[152:155], v[220:223]
	v_mfma_f32_16x16x32_bf16 v[52:55], v[232:235], v[152:155], v[184:187]
	v_add_u32_e32 v149, s14, v157
	v_cmp_lt_i32_e32 vcc, v149, v156
	v_lshlrev_b32_e32 v154, 1, v140
	v_lshlrev_b32_e32 v152, 1, v142
	s_and_saveexec_b64 s[8:9], vcc
	s_cbranch_execz .LBB0_2487
	v_add_u32_e32 v164, v141, v149
	v_ashrrev_i32_e32 v165, 31, v164
	v_readlane_b32 s10, v254, 3
	v_lshlrev_b64 v[164:165], 11, v[164:165]
	v_readlane_b32 s11, v254, 4
	v_mov_b32_e32 v155, v133
	v_mov_b32_e32 v153, v133
	v_lshl_add_u64 v[164:165], s[10:11], 0, v[164:165]
	v_lshl_add_u64 v[164:165], s[6:7], 1, v[164:165]
	v_lshl_add_u64 v[164:165], v[164:165], 0, v[154:155]
	v_lshl_add_u64 v[164:165], v[164:165], 0, v[152:153]
	v_cvt_pk_bf16_f32 v124, v124, v125
	v_cvt_pk_bf16_f32 v125, v126, v127
	v_cvt_pk_bf16_f32 v126, v128, v129
	v_cvt_pk_bf16_f32 v127, v130, v131
	v_cvt_pk_bf16_f32 v120, v120, v121
	v_cvt_pk_bf16_f32 v121, v122, v123
	v_cvt_pk_bf16_f32 v122, v116, v117
	v_cvt_pk_bf16_f32 v123, v118, v119
	global_store_dwordx4 v[164:165], v[124:127], off
	global_store_dwordx4 v[164:165], v[120:123], off offset:16
